# one-atomic quota reservation with 3600 + 1800 tiles deferred, idle-slot quotas 7/10/9/11
# speedup vs baseline: 1.0011x; 1.0011x over previous
; __device__ __forceinline__ void bt_load(const float* __restrict__ src, int N, int perm, int it, int ntn, f32x4 (&v)[8]) {
;     const int wid = threadIdx.x >> 6, lane = threadIdx.x & 63;
;     const int per = 16 * ntn, z = it / per, r = it % per, kt = r / ntn, nt = r % ntn;
;     const int np = nt * 256 + lane * 4;
;     const int sc = perm ? (nt * 128 + (lane & 31) * 4 + (lane >> 5) * 1024) : np;
;     const float* p = src + (size_t)z * 1024 * N + (size_t)(kt * 64 + wid * 8) * N + sc;
; #pragma unroll
;     for (int i = 0; i < 8; ++i) v[i] = __builtin_nontemporal_load((const f32x4*)(p + (size_t)i * N));
; }
; __device__ __forceinline__ void ph_big_transpose(const float* __restrict__ src, int N, int perm, int batch, bf16* __restrict__ dst, float* tile  , int G, int ndefer) {
;     const int tid = threadIdx.x, wid = tid >> 6, lane = tid & 63, ntn = N / 256, total = batch * 16 * ntn - ndefer;
;     int it = (int)blockIdx.x;
;     if (it >= total) return;
;     f32x4 cur[8], nxt[8], nx2[8];
;     bt_load(src, N, perm, it, ntn, cur);
;     if (it + G < total) bt_load(src, N, perm, it + G, ntn, nxt);
;     for (; it < total; it += G) {
;         const bool more = it + G < total, more2 = it + 2 * G < total;
;         if (more2) bt_load(src, N, perm, it + 2 * G, ntn, nx2);
.LBB0_63:
	s_cmpk_gt_i32 s2, 0x11ef
	s_waitcnt lgkmcnt(0)
	s_barrier
	s_cbranch_scc1 .LBB0_71
	s_ashr_i32 s0, s2, 31
	s_lshr_b32 s0, s0, 25
	s_add_i32 s1, s2, s0
	s_ashr_i32 s0, s1, 7
	s_and_b32 s1, s1, 0xff80
	s_sub_i32 s1, s2, s1
	s_bfe_i32 s4, s1, 0x80000
	s_bfe_u32 s4, s4, 0x3000c
	s_add_i32 s4, s1, s4
	s_bfe_i32 s5, s4, 0x80000
	s_and_b32 s4, s4, 0xf8
	v_lshlrev_b32_e32 v2, 2, v0
	s_sub_i32 s1, s1, s4
	v_and_b32_e32 v2, 0x7c, v2
	v_lshlrev_b32_e32 v3, 5, v0
	s_movk_i32 s4, 0x400
	s_sext_i32_i8 s1, s1
	v_and_or_b32 v99, v3, s4, v2
	v_lshl_add_u32 v2, s1, 7, v99
	s_ashr_i32 s1, s0, 31
	s_lshl_b64 s[0:1], s[0:1], 23
	s_sext_i32_i16 s5, s5
	s_add_u32 s0, s68, s0
	s_addc_u32 s1, s69, s1
	s_lshl_b32 s4, s5, 3
	v_lshrrev_b32_e32 v3, 3, v0
	s_andn2_b32 s4, s4, 63
	v_and_b32_e32 v110, 56, v3
	v_or_b32_e32 v4, s4, v110
	v_ashrrev_i32_e32 v5, 31, v4
	v_lshlrev_b64 v[4:5], 13, v[4:5]
	v_lshl_add_u64 v[4:5], s[0:1], 0, v[4:5]
	v_ashrrev_i32_e32 v3, 31, v2
	v_lshl_add_u64 v[2:3], v[2:3], 2, v[4:5]
	s_movk_i32 s0, 0x2000
	v_add_co_u32_e32 v4, vcc, s0, v2
	s_movk_i32 s1, 0x4000
	s_nop 0
	v_addc_co_u32_e32 v5, vcc, 0, v3, vcc
	global_load_dwordx4 v[38:41], v[2:3], off nt
	global_load_dwordx4 v[34:37], v[4:5], off nt
	v_add_co_u32_e32 v4, vcc, s1, v2
	s_movk_i32 s4, 0x6000
	s_nop 0
	v_addc_co_u32_e32 v5, vcc, 0, v3, vcc
	v_add_co_u32_e32 v6, vcc, s4, v2
	s_mov_b32 s5, 0x8000
	s_nop 0
	v_addc_co_u32_e32 v7, vcc, 0, v3, vcc
	global_load_dwordx4 v[46:49], v[4:5], off nt
	global_load_dwordx4 v[42:45], v[6:7], off nt
	v_add_co_u32_e32 v4, vcc, s5, v2
	s_mov_b32 s6, 0xa000
	s_nop 0
	v_addc_co_u32_e32 v5, vcc, 0, v3, vcc
	v_add_co_u32_e32 v6, vcc, s6, v2
	s_add_i32 s6, s62, s2
	s_nop 0
	v_addc_co_u32_e32 v7, vcc, 0, v3, vcc
	global_load_dwordx4 v[54:57], v[4:5], off nt
	global_load_dwordx4 v[50:53], v[6:7], off nt
	v_add_co_u32_e32 v4, vcc, 0xc000, v2
	s_cmpk_gt_i32 s6, 0x11ef
	s_nop 0
	v_addc_co_u32_e32 v5, vcc, 0, v3, vcc
	v_add_co_u32_e32 v2, vcc, 0xe000, v2
	s_nop 1
	v_addc_co_u32_e32 v3, vcc, 0, v3, vcc
	global_load_dwordx4 v[62:65], v[4:5], off nt
	global_load_dwordx4 v[58:61], v[2:3], off nt
	s_cbranch_scc1 .LBB0_66
	s_ashr_i32 s7, s6, 31
	s_lshr_b32 s7, s7, 25
	s_add_i32 s7, s6, s7
	s_ashr_i32 s8, s7, 7
	s_and_b32 s7, s7, 0xff80
	s_sub_i32 s6, s6, s7
	s_bfe_i32 s7, s6, 0x80000
	s_bfe_u32 s7, s7, 0x3000c
	s_add_i32 s7, s6, s7
	s_bfe_i32 s9, s7, 0x80000
	s_and_b32 s7, s7, 0xf8
	s_sub_i32 s6, s6, s7
	s_sext_i32_i16 s10, s9
	s_sext_i32_i8 s6, s6
	s_ashr_i32 s9, s8, 31
	v_lshl_add_u32 v2, s6, 7, v99
	s_lshl_b64 s[6:7], s[8:9], 23
	s_add_u32 s6, s68, s6
	s_addc_u32 s7, s69, s7
	s_lshl_b32 s8, s10, 3
	s_andn2_b32 s8, s8, 63
	v_or_b32_e32 v4, s8, v110
	v_ashrrev_i32_e32 v5, 31, v4
	v_lshlrev_b64 v[4:5], 13, v[4:5]
	v_lshl_add_u64 v[4:5], s[6:7], 0, v[4:5]
	v_ashrrev_i32_e32 v3, 31, v2
	v_lshl_add_u64 v[26:27], v[2:3], 2, v[4:5]
	v_add_co_u32_e32 v6, vcc, s0, v26
	s_nop 1
	v_addc_co_u32_e32 v7, vcc, 0, v27, vcc
	v_add_co_u32_e32 v10, vcc, s1, v26
	global_load_dwordx4 v[2:5], v[26:27], off nt
	s_nop 0
	global_load_dwordx4 v[6:9], v[6:7], off nt
	v_addc_co_u32_e32 v11, vcc, 0, v27, vcc
	v_add_co_u32_e32 v14, vcc, s4, v26
	s_nop 1
	v_addc_co_u32_e32 v15, vcc, 0, v27, vcc
	v_add_co_u32_e32 v18, vcc, s5, v26
	global_load_dwordx4 v[10:13], v[10:11], off nt
	s_nop 0
	global_load_dwordx4 v[14:17], v[14:15], off nt
	v_addc_co_u32_e32 v19, vcc, 0, v27, vcc
	v_add_co_u32_e32 v22, vcc, 0xa000, v26
	s_nop 1
	v_addc_co_u32_e32 v23, vcc, 0, v27, vcc
	v_add_co_u32_e32 v28, vcc, 0xc000, v26
	global_load_dwordx4 v[18:21], v[18:19], off nt
	s_nop 0
	global_load_dwordx4 v[22:25], v[22:23], off nt
	v_addc_co_u32_e32 v29, vcc, 0, v27, vcc
	v_add_co_u32_e32 v30, vcc, 0xe000, v26
	s_nop 1
	v_addc_co_u32_e32 v31, vcc, 0, v27, vcc
	global_load_dwordx4 v[26:29], v[28:29], off nt
	s_nop 0
	global_load_dwordx4 v[30:33], v[30:31], off nt

; __device__ __forceinline__ unsigned g8_cvt_pk(float lo, float hi) { unsigned r; asm volatile("v_cvt_pk_bf16_f32 %0, %1, %2" : "=v"(r) : "v"(lo), "v"(hi)); return r; }
; __device__ __forceinline__ void ph_big_transpose(const float* __restrict__ src, int N, int perm, int batch, bf16* __restrict__ dst, float* tile  , int G, int ndefer) {
;     ...
;     for (; it < total; it += G) {
;         const bool more = it + G < total, more2 = it + 2 * G < total;
;         if (more2) bt_load(src, N, perm, it + 2 * G, ntn, nx2);
;         __syncthreads();
; #pragma unroll
;         for (int i = 0; i < 8; ++i) { float* t = tile + (wid * 8 + i) * 257 + lane * 4; t[0] = cur[i][0]; t[1] = cur[i][1]; t[2] = cur[i][2]; t[3] = cur[i][3]; }
;         __syncthreads();
;         const int per = 16 * ntn, z = it / per, r = it % per, kt = r / ntn, nt = r % ntn;
;         bf16* d = dst + (size_t)z * N * 1024 + (((size_t)nt * 16 + kt) << 14);
;         const int kc = lane & 7;
; #pragma unroll
;         for (int pss = 0; pss < 4; ++pss) {
;             const int n = wid * 32 + pss * 8 + (lane >> 3); float f[8];
; #pragma unroll
;             for (int j = 0; j < 8; ++j) f[j] = tile[(kc * 8 + j) * 257 + n];
;             u32x4 w; w.x = g8_cvt_pk(f[0], f[1]); w.y = g8_cvt_pk(f[2], f[3]); w.z = g8_cvt_pk(f[4], f[5]); w.w = g8_cvt_pk(f[6], f[7]);
;             __builtin_nontemporal_store(w, (u32x4*)(d + n * 64 + kc * 8));
;         }
;         if (more) {
; #pragma unroll
;             for (int i = 0; i < 8; ++i) { cur[i] = nxt[i]; nxt[i] = nx2[i]; } }
;     }
.LBB0_67:
	s_barrier
	s_waitcnt vmcnt(7)
	ds_write_b128 v111, v[38:41]
	v_add_u32_e32 v38, 0x404, v111
	s_ashr_i32 s9, s8, 31
	s_waitcnt vmcnt(6)
	ds_write2_b32 v38, v34, v35 offset1:1
	v_add_u32_e32 v34, 0x40c, v111
	s_lshr_b32 s9, s9, 25
	ds_write2_b32 v34, v36, v37 offset1:1
	v_add_u32_e32 v34, 0x808, v111
	s_add_i32 s9, s8, s9
	s_waitcnt vmcnt(5)
	ds_write2_b64 v34, v[46:47], v[48:49] offset1:1
	v_add_u32_e32 v34, 0xc0c, v111
	s_ashr_i32 s10, s9, 7
	s_and_b32 s9, s9, 0xff80
	s_waitcnt vmcnt(4)
	ds_write2_b32 v34, v42, v43 offset1:1
	v_add_u32_e32 v34, 0xc14, v111
	s_sub_i32 s9, s8, s9
	s_add_i32 s31, s8, s62
	ds_write2_b32 v34, v44, v45 offset1:1
	s_waitcnt vmcnt(3)
	ds_write_b128 v111, v[54:57] offset:4112
	v_add_u32_e32 v34, 0x1414, v111
	s_bfe_i32 s8, s9, 0x80000
	s_waitcnt vmcnt(2)
	ds_write2_b32 v34, v50, v51 offset1:1
	v_add_u32_e32 v34, 0x141c, v111
	s_bfe_u32 s8, s8, 0x3000c
	ds_write2_b32 v34, v52, v53 offset1:1
	v_add_u32_e32 v34, 0x1818, v111
	s_add_i32 s11, s9, s8
	s_waitcnt vmcnt(1)
	ds_write2_b64 v34, v[62:63], v[64:65] offset1:1
	v_add_u32_e32 v34, 0x1c1c, v111
	s_bfe_i32 s8, s11, 0x80000
	s_and_b32 s11, s11, 0xf8
	s_waitcnt vmcnt(0)
	ds_write2_b32 v34, v58, v59 offset1:1
	v_add_u32_e32 v34, 0x1c24, v111
	s_sext_i32_i16 s8, s8
	s_sub_i32 s30, s9, s11
	s_ashr_i32 s11, s10, 31
	ds_write2_b32 v34, v60, v61 offset1:1
	s_waitcnt lgkmcnt(0)
	s_barrier
	s_lshr_b32 s8, s8, 3
	s_lshl_b64 s[10:11], s[10:11], 22
	ds_read_b32 v34, v112 offset:1028
	ds_read_b32 v35, v112 offset:3084
	ds_read_b32 v36, v112 offset:5140
	ds_read_b32 v37, v112 offset:7196
	ds_read_b32 v38, v112 offset:6168
	ds_read_b32 v39, v112 offset:4112
	ds_read_b32 v40, v112 offset:2056
	ds_read_b32 v41, v112
	s_add_u32 s33, s5, s10
	s_addc_u32 s34, s6, s11
	s_bfe_i64 s[10:11], s[30:31], 0x80000
	s_bfe_i64 s[8:9], s[8:9], 0x100000
	s_lshl_b64 s[10:11], s[10:11], 19
	s_add_u32 s10, s33, s10
	s_addc_u32 s11, s34, s11
	s_lshl_b64 s[8:9], s[8:9], 15
	s_waitcnt lgkmcnt(0)
	v_cvt_pk_bf16_f32 v34, v41, v34
	v_cvt_pk_bf16_f32 v35, v40, v35
	v_cvt_pk_bf16_f32 v36, v39, v36
	v_cvt_pk_bf16_f32 v37, v38, v37
	ds_read_b32 v42, v112 offset:1060
	ds_read_b32 v43, v112 offset:3116
	ds_read_b32 v44, v112 offset:5172
	ds_read_b32 v45, v112 offset:7228
	ds_read_b32 v46, v112 offset:6200
	ds_read_b32 v47, v112 offset:4144
	ds_read_b32 v48, v112 offset:2088
	ds_read_b32 v49, v112 offset:32
	s_add_u32 s8, s10, s8
	s_addc_u32 s9, s11, s9
	v_lshl_add_u64 v[38:39], s[8:9], 0, v[100:101]
	v_mov_b32_e32 v103, v101
	v_lshl_add_u64 v[40:41], v[38:39], 0, v[102:103]
	global_store_dwordx4 v[40:41], v[34:37], off nt
	v_mov_b32_e32 v105, v101
	v_lshl_add_u64 v[40:41], v[38:39], 0, v[104:105]
	s_waitcnt lgkmcnt(0)
	v_cvt_pk_bf16_f32 v34, v49, v42
	v_cvt_pk_bf16_f32 v35, v48, v43
	v_cvt_pk_bf16_f32 v36, v47, v44
	v_cvt_pk_bf16_f32 v37, v46, v45
	ds_read_b32 v42, v112 offset:1092
	ds_read_b32 v43, v112 offset:3148
	ds_read_b32 v44, v112 offset:5204
	ds_read_b32 v45, v112 offset:6232
	ds_read_b32 v46, v112 offset:4176
	ds_read_b32 v47, v112 offset:2120
	ds_read_b32 v48, v112 offset:64
	ds_read_b32 v49, v112 offset:7260
	global_store_dwordx4 v[40:41], v[34:37], off nt
	v_mov_b32_e32 v107, v101
	v_lshl_add_u64 v[40:41], v[38:39], 0, v[106:107]
	s_waitcnt lgkmcnt(1)
	v_cvt_pk_bf16_f32 v34, v48, v42
	v_cvt_pk_bf16_f32 v35, v47, v43
	v_cvt_pk_bf16_f32 v36, v46, v44
	s_waitcnt lgkmcnt(0)
	v_cvt_pk_bf16_f32 v37, v45, v49
	ds_read_b32 v42, v112 offset:1124
	ds_read_b32 v43, v112 offset:3180
	ds_read_b32 v44, v112 offset:5236
	ds_read_b32 v45, v112 offset:6264
	ds_read_b32 v46, v112 offset:4208
	ds_read_b32 v47, v112 offset:2152
	ds_read_b32 v48, v112 offset:96
	ds_read_b32 v49, v112 offset:7292
	v_mov_b32_e32 v109, v101
	global_store_dwordx4 v[40:41], v[34:37], off nt
	v_lshl_add_u64 v[38:39], v[38:39], 0, v[108:109]
	v_mov_b64_e32 v[60:61], v[32:33]
	s_waitcnt lgkmcnt(1)
	v_cvt_pk_bf16_f32 v34, v48, v42
	v_cvt_pk_bf16_f32 v35, v47, v43
	v_cvt_pk_bf16_f32 v36, v46, v44
	s_waitcnt lgkmcnt(0)
	v_cvt_pk_bf16_f32 v37, v45, v49
	global_store_dwordx4 v[38:39], v[34:37], off nt
	v_mov_b64_e32 v[64:65], v[28:29]
	v_mov_b64_e32 v[52:53], v[24:25]
	v_mov_b64_e32 v[56:57], v[20:21]
	v_mov_b64_e32 v[44:45], v[16:17]
	v_mov_b64_e32 v[48:49], v[12:13]
	v_mov_b64_e32 v[36:37], v[8:9]
	v_mov_b64_e32 v[40:41], v[4:5]
	v_mov_b64_e32 v[58:59], v[30:31]
	v_mov_b64_e32 v[62:63], v[26:27]
	v_mov_b64_e32 v[50:51], v[22:23]
	v_mov_b64_e32 v[54:55], v[18:19]
	v_mov_b64_e32 v[42:43], v[14:15]
	v_mov_b64_e32 v[46:47], v[10:11]
	v_mov_b64_e32 v[34:35], v[6:7]
	v_mov_b64_e32 v[38:39], v[2:3]
	v_mov_b64_e32 v[30:31], v[94:95]
	v_mov_b64_e32 v[26:27], v[90:91]
	v_mov_b64_e32 v[22:23], v[86:87]
	v_mov_b64_e32 v[18:19], v[82:83]
	v_mov_b64_e32 v[14:15], v[78:79]
	v_mov_b64_e32 v[10:11], v[74:75]
	v_mov_b64_e32 v[6:7], v[70:71]
	v_mov_b64_e32 v[2:3], v[66:67]
	s_cmpk_lt_i32 s31, 0x11f0
	v_mov_b64_e32 v[32:33], v[96:97]
	v_mov_b64_e32 v[28:29], v[92:93]
	v_mov_b64_e32 v[24:25], v[88:89]
	v_mov_b64_e32 v[20:21], v[84:85]
	v_mov_b64_e32 v[16:17], v[80:81]
	v_mov_b64_e32 v[12:13], v[76:77]
	v_mov_b64_e32 v[8:9], v[72:73]
	v_mov_b64_e32 v[4:5], v[68:69]
	s_mov_b32 s8, s31
	s_cbranch_scc0 .LBB0_70
; __device__ __forceinline__ void bt_load(const float* __restrict__ src, int N, int perm, int it, int ntn, f32x4 (&v)[8]) {
;     const int wid = threadIdx.x >> 6, lane = threadIdx.x & 63;
;     const int per = 16 * ntn, z = it / per, r = it % per, kt = r / ntn, nt = r % ntn;
;     const int np = nt * 256 + lane * 4;
;     const int sc = perm ? (nt * 128 + (lane & 31) * 4 + (lane >> 5) * 1024) : np;
;     const float* p = src + (size_t)z * 1024 * N + (size_t)(kt * 64 + wid * 8) * N + sc;
; #pragma unroll
;     for (int i = 0; i < 8; ++i) v[i] = __builtin_nontemporal_load((const f32x4*)(p + (size_t)i * N));
; }
; __device__ __forceinline__ void ph_big_transpose(const float* __restrict__ src, int N, int perm, int batch, bf16* __restrict__ dst, float* tile  , int G, int ndefer) {
;     const int tid = threadIdx.x, wid = tid >> 6, lane = tid & 63, ntn = N / 256, total = batch * 16 * ntn - ndefer;
;     int it = (int)blockIdx.x;
;     if (it >= total) return;
;     f32x4 cur[8], nxt[8], nx2[8];
;     bt_load(src, N, perm, it, ntn, cur);
;     if (it + G < total) bt_load(src, N, perm, it + G, ntn, nxt);
;     for (; it < total; it += G) {
;         const bool more = it + G < total, more2 = it + 2 * G < total;
;         if (more2) bt_load(src, N, perm, it + 2 * G, ntn, nx2);
.LBB0_68:
	s_add_i32 s9, s7, s8
	s_cmpk_gt_i32 s9, 0x11ef
	s_cbranch_scc1 .LBB0_67
	s_ashr_i32 s10, s9, 31
	s_lshr_b32 s10, s10, 25
	s_add_i32 s11, s9, s10
	s_ashr_i32 s10, s11, 7
	s_and_b32 s11, s11, 0xff80
	s_sub_i32 s9, s9, s11
	s_bfe_i32 s11, s9, 0x80000
	s_bfe_u32 s11, s11, 0x3000c
	s_add_i32 s11, s9, s11
	s_bfe_i32 s30, s11, 0x80000
	s_and_b32 s11, s11, 0xf8
	s_sub_i32 s9, s9, s11
	s_ashr_i32 s11, s10, 31
	s_lshl_b64 s[10:11], s[10:11], 23
	s_sext_i32_i16 s30, s30
	s_sext_i32_i8 s9, s9
	s_add_u32 s10, s68, s10
	v_lshl_add_u32 v66, s9, 7, v99
	s_addc_u32 s11, s69, s11
	s_lshl_b32 s9, s30, 3
	s_andn2_b32 s9, s9, 63
	v_or_b32_e32 v68, s9, v110
	v_ashrrev_i32_e32 v69, 31, v68
	v_lshlrev_b64 v[68:69], 13, v[68:69]
	v_lshl_add_u64 v[68:69], s[10:11], 0, v[68:69]
	v_ashrrev_i32_e32 v67, 31, v66
	v_lshl_add_u64 v[90:91], v[66:67], 2, v[68:69]
	v_add_co_u32_e32 v70, vcc, s0, v90
	s_nop 1
	v_addc_co_u32_e32 v71, vcc, 0, v91, vcc
	v_add_co_u32_e32 v74, vcc, s1, v90
	global_load_dwordx4 v[66:69], v[90:91], off nt
	s_nop 0
	global_load_dwordx4 v[70:73], v[70:71], off nt
	v_addc_co_u32_e32 v75, vcc, 0, v91, vcc
	v_add_co_u32_e32 v78, vcc, s4, v90
	s_nop 1
	v_addc_co_u32_e32 v79, vcc, 0, v91, vcc
	v_add_co_u32_e32 v82, vcc, 0x8000, v90
	global_load_dwordx4 v[74:77], v[74:75], off nt
	s_nop 0
	global_load_dwordx4 v[78:81], v[78:79], off nt
	v_addc_co_u32_e32 v83, vcc, 0, v91, vcc
	v_add_co_u32_e32 v86, vcc, 0xa000, v90
	s_nop 1
	v_addc_co_u32_e32 v87, vcc, 0, v91, vcc
	v_add_co_u32_e32 v92, vcc, 0xc000, v90
	global_load_dwordx4 v[82:85], v[82:83], off nt
	s_nop 0
	global_load_dwordx4 v[86:89], v[86:87], off nt
	v_addc_co_u32_e32 v93, vcc, 0, v91, vcc
	v_add_co_u32_e32 v94, vcc, 0xe000, v90
	s_nop 1
	v_addc_co_u32_e32 v95, vcc, 0, v91, vcc
	global_load_dwordx4 v[90:93], v[92:93], off nt
	s_nop 0
	global_load_dwordx4 v[94:97], v[94:95], off nt
	s_branch .LBB0_67

; __device__ __forceinline__ void bt_load(const float* __restrict__ src, int N, int perm, int it, int ntn, f32x4 (&v)[8]) {
;     const int wid = threadIdx.x >> 6, lane = threadIdx.x & 63;
;     const int per = 16 * ntn, z = it / per, r = it % per, kt = r / ntn, nt = r % ntn;
;     const int np = nt * 256 + lane * 4;
;     const int sc = perm ? (nt * 128 + (lane & 31) * 4 + (lane >> 5) * 1024) : np;
;     const float* p = src + (size_t)z * 1024 * N + (size_t)(kt * 64 + wid * 8) * N + sc;
; #pragma unroll
;     for (int i = 0; i < 8; ++i) v[i] = __builtin_nontemporal_load((const f32x4*)(p + (size_t)i * N));
; }
; __device__ __forceinline__ void ph_big_transpose(const float* __restrict__ src, int N, int perm, int batch, bf16* __restrict__ dst, float* tile  , int G, int ndefer) {
;     const int tid = threadIdx.x, wid = tid >> 6, lane = tid & 63, ntn = N / 256, total = batch * 16 * ntn - ndefer;
;     int it = (int)blockIdx.x;
;     if (it >= total) return;
;     f32x4 cur[8], nxt[8], nx2[8];
;     bt_load(src, N, perm, it, ntn, cur);
;     if (it + G < total) bt_load(src, N, perm, it + G, ntn, nxt);
.LBB0_71:
	s_cmpk_gt_i32 s2, 0x8f7
	s_cbranch_scc1 .LBB0_79
	s_ashr_i32 s0, s2, 31
	s_lshr_b32 s0, s0, 26
	s_add_i32 s1, s2, s0
	s_ashr_i32 s0, s1, 6
	s_and_b32 s1, s1, 0xffc0
	s_sub_i32 s1, s2, s1
	s_bfe_i32 s4, s1, 0x80000
	s_bfe_u32 s4, s4, 0x2000d
	s_add_i32 s4, s1, s4
	s_bfe_i32 s5, s4, 0x80000
	s_and_b32 s4, s4, 0xfc
	s_sub_i32 s1, s1, s4
	v_lshlrev_b32_e32 v2, 2, v0
	s_sext_i32_i8 s1, s1
	v_and_b32_e32 v99, 0xfc, v2
	v_lshl_or_b32 v2, s1, 8, v99
	s_ashr_i32 s1, s0, 31
	s_lshl_b64 s[0:1], s[0:1], 22
	s_sext_i32_i16 s5, s5
	s_add_u32 s0, s72, s0
	s_addc_u32 s1, s73, s1
	s_lshl_b32 s4, s5, 4
	v_lshrrev_b32_e32 v3, 3, v0
	s_andn2_b32 s4, s4, 63
	v_and_b32_e32 v110, 56, v3
	v_or_b32_e32 v4, s4, v110
	v_ashrrev_i32_e32 v5, 31, v4
	v_lshlrev_b64 v[4:5], 12, v[4:5]
	v_lshl_add_u64 v[4:5], s[0:1], 0, v[4:5]
	v_ashrrev_i32_e32 v3, 31, v2
	v_lshl_add_u64 v[2:3], v[2:3], 2, v[4:5]
	s_movk_i32 s0, 0x2000
	v_add_co_u32_e32 v4, vcc, s0, v2
	s_movk_i32 s4, 0x4000
	s_nop 0
	v_addc_co_u32_e32 v5, vcc, 0, v3, vcc
	global_load_dwordx4 v[42:45], v[4:5], off offset:-4096 nt
	global_load_dwordx4 v[34:37], v[4:5], off nt
	v_add_co_u32_e32 v4, vcc, s4, v2
	s_movk_i32 s1, 0x5000
	s_nop 0
	v_addc_co_u32_e32 v5, vcc, 0, v3, vcc
	global_load_dwordx4 v[46:49], v[4:5], off offset:-4096 nt
	global_load_dwordx4 v[38:41], v[4:5], off nt
	v_add_co_u32_e32 v4, vcc, s1, v2
	s_add_i32 s5, s62, s2
	s_nop 0
	v_addc_co_u32_e32 v5, vcc, 0, v3, vcc
	global_load_dwordx4 v[62:65], v[2:3], off nt
	global_load_dwordx4 v[50:53], v[4:5], off nt
	v_add_co_u32_e32 v4, vcc, 0x6000, v2
	s_cmpk_gt_i32 s5, 0x8f7
	s_nop 0
	v_addc_co_u32_e32 v5, vcc, 0, v3, vcc
	v_add_co_u32_e32 v2, vcc, 0x7000, v2
	s_movk_i32 s1, 0x3000
	s_nop 0
	v_addc_co_u32_e32 v3, vcc, 0, v3, vcc
	global_load_dwordx4 v[58:61], v[4:5], off nt
	global_load_dwordx4 v[54:57], v[2:3], off nt
	s_cbranch_scc1 .LBB0_74
	s_ashr_i32 s6, s5, 31
	s_lshr_b32 s6, s6, 26
	s_add_i32 s7, s5, s6
	s_ashr_i32 s6, s7, 6
	s_and_b32 s7, s7, 0xffc0
	s_sub_i32 s5, s5, s7
	s_bfe_i32 s7, s5, 0x80000
	s_bfe_u32 s7, s7, 0x2000d
	s_add_i32 s7, s5, s7
	s_bfe_i32 s8, s7, 0x80000
	s_and_b32 s7, s7, 0xfc
	s_sub_i32 s5, s5, s7
	s_ashr_i32 s7, s6, 31
	s_lshl_b64 s[6:7], s[6:7], 22
	s_sext_i32_i16 s8, s8
	s_sext_i32_i8 s5, s5
	s_add_u32 s6, s72, s6
	v_lshl_or_b32 v2, s5, 8, v99
	s_addc_u32 s7, s73, s7
	s_lshl_b32 s5, s8, 4
	s_andn2_b32 s5, s5, 63
	v_or_b32_e32 v4, s5, v110
	v_ashrrev_i32_e32 v5, 31, v4
	v_lshlrev_b64 v[4:5], 12, v[4:5]
	v_lshl_add_u64 v[4:5], s[6:7], 0, v[4:5]
	v_ashrrev_i32_e32 v3, 31, v2
	v_lshl_add_u64 v[26:27], v[2:3], 2, v[4:5]
	v_add_co_u32_e32 v2, vcc, s0, v26
	s_nop 1
	v_addc_co_u32_e32 v3, vcc, 0, v27, vcc
	v_add_co_u32_e32 v10, vcc, s4, v26
	global_load_dwordx4 v[6:9], v[2:3], off offset:-4096 nt
	s_nop 0
	global_load_dwordx4 v[2:5], v[2:3], off nt
	v_addc_co_u32_e32 v11, vcc, 0, v27, vcc
	v_add_co_u32_e32 v18, vcc, 0x5000, v26
	global_load_dwordx4 v[14:17], v[10:11], off offset:-4096 nt
	s_nop 0
	global_load_dwordx4 v[10:13], v[10:11], off nt
	v_addc_co_u32_e32 v19, vcc, 0, v27, vcc
	v_add_co_u32_e32 v28, vcc, 0x6000, v26
	global_load_dwordx4 v[22:25], v[26:27], off nt
	s_nop 0
	global_load_dwordx4 v[18:21], v[18:19], off nt
	v_addc_co_u32_e32 v29, vcc, 0, v27, vcc
	v_add_co_u32_e32 v30, vcc, 0x7000, v26
	s_nop 1
	v_addc_co_u32_e32 v31, vcc, 0, v27, vcc
	global_load_dwordx4 v[26:29], v[28:29], off nt
	s_nop 0
	global_load_dwordx4 v[30:33], v[30:31], off nt

; __device__ __forceinline__ void bt_load(const float* __restrict__ src, int N, int perm, int it, int ntn, f32x4 (&v)[8]) {
;     const int wid = threadIdx.x >> 6, lane = threadIdx.x & 63;
;     const int per = 16 * ntn, z = it / per, r = it % per, kt = r / ntn, nt = r % ntn;
;     const int np = nt * 256 + lane * 4;
;     const int sc = perm ? (nt * 128 + (lane & 31) * 4 + (lane >> 5) * 1024) : np;
;     const float* p = src + (size_t)z * 1024 * N + (size_t)(kt * 64 + wid * 8) * N + sc;
; #pragma unroll
;     for (int i = 0; i < 8; ++i) v[i] = __builtin_nontemporal_load((const f32x4*)(p + (size_t)i * N));
; }
; __device__ __forceinline__ void ph_big_transpose(const float* __restrict__ src, int N, int perm, int batch, bf16* __restrict__ dst, float* tile  , int G, int ndefer) {
;     const int tid = threadIdx.x, wid = tid >> 6, lane = tid & 63, ntn = N / 256, total = batch * 16 * ntn - ndefer;
;     int it = (int)blockIdx.x;
;     if (it >= total) return;
;     f32x4 cur[8], nxt[8], nx2[8];
;     bt_load(src, N, perm, it, ntn, cur);
;     if (it + G < total) bt_load(src, N, perm, it + G, ntn, nxt);
;     for (; it < total; it += G) {
;         const bool more = it + G < total, more2 = it + 2 * G < total;
;         if (more2) bt_load(src, N, perm, it + 2 * G, ntn, nx2);
;         __syncthreads();
; #pragma unroll
;         for (int i = 0; i < 8; ++i) { float* t = tile + (wid * 8 + i) * 257 + lane * 4; t[0] = cur[i][0]; t[1] = cur[i][1]; t[2] = cur[i][2]; t[3] = cur[i][3]; }
;         __syncthreads();
;         const int per = 16 * ntn, z = it / per, r = it % per, kt = r / ntn, nt = r % ntn;
;         bf16* d = dst + (size_t)z * N * 1024 + (((size_t)nt * 16 + kt) << 14);
;         const int kc = lane & 7;
; #pragma unroll
;         for (int pss = 0; pss < 4; ++pss) {
;             const int n = wid * 32 + pss * 8 + (lane >> 3); float f[8];
; #pragma unroll
;             for (int j = 0; j < 8; ++j) f[j] = tile[(kc * 8 + j) * 257 + n];
;             u32x4 w; w.x = g8_cvt_pk(f[0], f[1]); w.y = g8_cvt_pk(f[2], f[3]); w.z = g8_cvt_pk(f[4], f[5]); w.w = g8_cvt_pk(f[6], f[7]);
;             __builtin_nontemporal_store(w, (u32x4*)(d + n * 64 + kc * 8));
;         }
;         if (more) {
; #pragma unroll
;             for (int i = 0; i < 8; ++i) { cur[i] = nxt[i]; nxt[i] = nx2[i]; } }
;     }
.LBB0_75:
	s_ashr_i32 s8, s3, 31
	s_barrier
	s_waitcnt vmcnt(3)
	ds_write_b128 v111, v[62:65]
	v_add_u32_e32 v62, 0x404, v111
	s_lshr_b32 s8, s8, 26
	ds_write2_b32 v62, v42, v43 offset1:1
	v_add_u32_e32 v42, 0x40c, v111
	s_add_i32 s9, s3, s8
	ds_write2_b32 v42, v44, v45 offset1:1
	v_add_u32_e32 v42, 0x808, v111
	s_ashr_i32 s8, s9, 6
	s_and_b32 s9, s9, 0xffc0
	s_add_i32 s7, s3, s62
	ds_write2_b64 v42, v[34:35], v[36:37] offset1:1
	v_add_u32_e32 v34, 0xc0c, v111
	s_sub_i32 s3, s3, s9
	ds_write2_b32 v34, v46, v47 offset1:1
	v_add_u32_e32 v34, 0xc14, v111
	s_bfe_i32 s9, s3, 0x80000
	ds_write2_b32 v34, v48, v49 offset1:1
	ds_write_b128 v111, v[38:41] offset:4112
	v_add_u32_e32 v34, 0x1414, v111
	s_bfe_u32 s9, s9, 0x2000d
	s_waitcnt vmcnt(2)
	ds_write2_b32 v34, v50, v51 offset1:1
	v_add_u32_e32 v34, 0x141c, v111
	s_add_i32 s9, s3, s9
	ds_write2_b32 v34, v52, v53 offset1:1
	v_add_u32_e32 v34, 0x1818, v111
	s_bfe_i32 s10, s9, 0x80000
	s_and_b32 s9, s9, 0xfc
	s_waitcnt vmcnt(1)
	ds_write2_b64 v34, v[58:59], v[60:61] offset1:1
	v_add_u32_e32 v34, 0x1c1c, v111
	s_sext_i32_i16 s10, s10
	s_sub_i32 s30, s3, s9
	s_ashr_i32 s9, s8, 31
	s_waitcnt vmcnt(0)
	ds_write2_b32 v34, v54, v55 offset1:1
	v_add_u32_e32 v34, 0x1c24, v111
	s_lshr_b32 s10, s10, 2
	s_lshl_b64 s[8:9], s[8:9], 21
	ds_write2_b32 v34, v56, v57 offset1:1
	s_waitcnt lgkmcnt(0)
	s_barrier
	s_add_u32 s3, s4, s8
	ds_read_b32 v34, v112 offset:1028
	ds_read_b32 v35, v112 offset:3084
	ds_read_b32 v36, v112 offset:5140
	ds_read_b32 v37, v112 offset:7196
	ds_read_b32 v38, v112 offset:6168
	ds_read_b32 v39, v112 offset:4112
	ds_read_b32 v40, v112 offset:2056
	ds_read_b32 v41, v112
	s_addc_u32 s31, s5, s9
	s_bfe_i64 s[8:9], s[30:31], 0x80000
	s_bfe_i64 s[10:11], s[10:11], 0x100000
	s_lshl_b64 s[8:9], s[8:9], 19
	s_add_u32 s3, s3, s8
	s_addc_u32 s30, s31, s9
	s_lshl_b64 s[8:9], s[10:11], 15
	s_waitcnt lgkmcnt(0)
	v_cvt_pk_bf16_f32 v34, v41, v34
	v_cvt_pk_bf16_f32 v35, v40, v35
	v_cvt_pk_bf16_f32 v36, v39, v36
	v_cvt_pk_bf16_f32 v37, v38, v37
	ds_read_b32 v42, v112 offset:1060
	ds_read_b32 v43, v112 offset:3116
	ds_read_b32 v44, v112 offset:5172
	ds_read_b32 v45, v112 offset:7228
	ds_read_b32 v46, v112 offset:6200
	ds_read_b32 v47, v112 offset:4144
	ds_read_b32 v48, v112 offset:2088
	ds_read_b32 v49, v112 offset:32
	s_add_u32 s8, s3, s8
	s_addc_u32 s9, s30, s9
	v_lshl_add_u64 v[38:39], s[8:9], 0, v[100:101]
	v_mov_b32_e32 v103, v101
	v_lshl_add_u64 v[40:41], v[38:39], 0, v[102:103]
	global_store_dwordx4 v[40:41], v[34:37], off nt
	v_mov_b32_e32 v105, v101
	v_lshl_add_u64 v[40:41], v[38:39], 0, v[104:105]
	s_waitcnt lgkmcnt(0)
	v_cvt_pk_bf16_f32 v34, v49, v42
	v_cvt_pk_bf16_f32 v35, v48, v43
	v_cvt_pk_bf16_f32 v36, v47, v44
	v_cvt_pk_bf16_f32 v37, v46, v45
	ds_read_b32 v42, v112 offset:1092
	ds_read_b32 v43, v112 offset:3148
	ds_read_b32 v44, v112 offset:5204
	ds_read_b32 v45, v112 offset:6232
	ds_read_b32 v46, v112 offset:4176
	ds_read_b32 v47, v112 offset:2120
	ds_read_b32 v48, v112 offset:64
	ds_read_b32 v49, v112 offset:7260
	global_store_dwordx4 v[40:41], v[34:37], off nt
	v_mov_b32_e32 v107, v101
	v_lshl_add_u64 v[40:41], v[38:39], 0, v[106:107]
	s_waitcnt lgkmcnt(1)
	v_cvt_pk_bf16_f32 v34, v48, v42
	v_cvt_pk_bf16_f32 v35, v47, v43
	v_cvt_pk_bf16_f32 v36, v46, v44
	s_waitcnt lgkmcnt(0)
	v_cvt_pk_bf16_f32 v37, v45, v49
	ds_read_b32 v42, v112 offset:1124
	ds_read_b32 v43, v112 offset:3180
	ds_read_b32 v44, v112 offset:5236
	ds_read_b32 v45, v112 offset:6264
	ds_read_b32 v46, v112 offset:4208
	ds_read_b32 v47, v112 offset:2152
	ds_read_b32 v48, v112 offset:96
	ds_read_b32 v49, v112 offset:7292
	v_mov_b32_e32 v109, v101
	global_store_dwordx4 v[40:41], v[34:37], off nt
	v_lshl_add_u64 v[38:39], v[38:39], 0, v[108:109]
	v_mov_b64_e32 v[56:57], v[32:33]
	s_waitcnt lgkmcnt(1)
	v_cvt_pk_bf16_f32 v34, v48, v42
	v_cvt_pk_bf16_f32 v35, v47, v43
	v_cvt_pk_bf16_f32 v36, v46, v44
	s_waitcnt lgkmcnt(0)
	v_cvt_pk_bf16_f32 v37, v45, v49
	global_store_dwordx4 v[38:39], v[34:37], off nt
	v_mov_b64_e32 v[60:61], v[28:29]
	v_mov_b64_e32 v[52:53], v[20:21]
	v_mov_b64_e32 v[40:41], v[12:13]
	v_mov_b64_e32 v[48:49], v[16:17]
	v_mov_b64_e32 v[36:37], v[4:5]
	v_mov_b64_e32 v[44:45], v[8:9]
	v_mov_b64_e32 v[64:65], v[24:25]
	v_mov_b64_e32 v[54:55], v[30:31]
	v_mov_b64_e32 v[58:59], v[26:27]
	v_mov_b64_e32 v[50:51], v[18:19]
	v_mov_b64_e32 v[38:39], v[10:11]
	v_mov_b64_e32 v[46:47], v[14:15]
	v_mov_b64_e32 v[34:35], v[2:3]
	v_mov_b64_e32 v[42:43], v[6:7]
	v_mov_b64_e32 v[62:63], v[22:23]
	v_mov_b64_e32 v[30:31], v[94:95]
	v_mov_b64_e32 v[26:27], v[90:91]
	v_mov_b64_e32 v[18:19], v[86:87]
	v_mov_b64_e32 v[10:11], v[82:83]
	v_mov_b64_e32 v[14:15], v[74:75]
	v_mov_b64_e32 v[2:3], v[66:67]
	v_mov_b64_e32 v[6:7], v[70:71]
	v_mov_b64_e32 v[22:23], v[78:79]
	s_cmpk_lt_i32 s7, 0x8f8
	v_mov_b64_e32 v[32:33], v[96:97]
	v_mov_b64_e32 v[28:29], v[92:93]
	v_mov_b64_e32 v[20:21], v[88:89]
	v_mov_b64_e32 v[12:13], v[84:85]
	v_mov_b64_e32 v[16:17], v[76:77]
	v_mov_b64_e32 v[4:5], v[68:69]
	v_mov_b64_e32 v[8:9], v[72:73]
	v_mov_b64_e32 v[24:25], v[80:81]
	s_mov_b32 s3, s7
	s_cbranch_scc0 .LBB0_78
.LBB0_76:
	s_add_i32 s7, s6, s3
	s_cmpk_gt_i32 s7, 0x8f7
	s_cbranch_scc1 .LBB0_75
	s_ashr_i32 s8, s7, 31
	s_lshr_b32 s8, s8, 26
	s_add_i32 s9, s7, s8
	s_ashr_i32 s8, s9, 6
	s_and_b32 s9, s9, 0xffc0
	s_sub_i32 s7, s7, s9
	s_bfe_i32 s9, s7, 0x80000
	s_bfe_u32 s9, s9, 0x2000d
	s_add_i32 s9, s7, s9
	s_bfe_i32 s10, s9, 0x80000
	s_and_b32 s9, s9, 0xfc
	s_sub_i32 s7, s7, s9
	s_ashr_i32 s9, s8, 31
	s_lshl_b64 s[8:9], s[8:9], 22
	s_sext_i32_i16 s10, s10
	s_sext_i32_i8 s7, s7
	s_add_u32 s8, s72, s8
	v_lshl_or_b32 v66, s7, 8, v99
	s_addc_u32 s9, s73, s9
	s_lshl_b32 s7, s10, 4
	s_andn2_b32 s7, s7, 63
	v_or_b32_e32 v68, s7, v110
	v_ashrrev_i32_e32 v69, 31, v68
	v_lshlrev_b64 v[68:69], 12, v[68:69]
	v_lshl_add_u64 v[68:69], s[8:9], 0, v[68:69]
	v_ashrrev_i32_e32 v67, 31, v66
	v_lshl_add_u64 v[90:91], v[66:67], 2, v[68:69]
	v_add_co_u32_e32 v66, vcc, s0, v90
	s_nop 1
	v_addc_co_u32_e32 v67, vcc, 0, v91, vcc
	v_add_co_u32_e32 v74, vcc, s1, v90
	global_load_dwordx4 v[70:73], v[66:67], off offset:-4096 nt
	s_nop 0
	global_load_dwordx4 v[66:69], v[66:67], off nt
	v_addc_co_u32_e32 v75, vcc, 0, v91, vcc
	v_add_co_u32_e32 v82, vcc, 0x4000, v90
	global_load_dwordx4 v[78:81], v[90:91], off nt
	s_nop 0
	global_load_dwordx4 v[74:77], v[74:75], off nt
	v_addc_co_u32_e32 v83, vcc, 0, v91, vcc
	v_add_co_u32_e32 v86, vcc, 0x5000, v90
	s_nop 1
	v_addc_co_u32_e32 v87, vcc, 0, v91, vcc
	v_add_co_u32_e32 v92, vcc, 0x6000, v90
	global_load_dwordx4 v[82:85], v[82:83], off nt
	s_nop 0
	global_load_dwordx4 v[86:89], v[86:87], off nt
	v_addc_co_u32_e32 v93, vcc, 0, v91, vcc
	v_add_co_u32_e32 v94, vcc, 0x7000, v90
	s_nop 1
	v_addc_co_u32_e32 v95, vcc, 0, v91, vcc
	global_load_dwordx4 v[90:93], v[92:93], off nt
	s_nop 0
	global_load_dwordx4 v[94:97], v[94:95], off nt
	s_branch .LBB0_75

; #define SEAM(k) do { if (IN(k) && IN((k) + 1)) xcd_barrier(bar); \
;         if (PROBE_MASK) { const unsigned long long t_ = __builtin_amdgcn_s_memrealtime(); if ((PROBE_MASK >> (k)) & 1u) pr_acc += t_ - pr_t0; pr_t0 = t_; } } while (0)
; __device__ __forceinline__ void convert_deferred(const Ptrs& P, unsigned char* lds, int quota) {
;     const int tid = threadIdx.x, wid = tid >> 6, lane = tid & 63;
;     float* tile = (float*)lds;
;     volatile __attribute__((address_space(3))) int* slot = (volatile __attribute__((address_space(3))) int*)((__attribute__((address_space(3))) unsigned char*)lds + 131072 + 320 + 11000);
;     unsigned* q = (unsigned*)(P.ws + WS_CTL) + CW_DEFQ;
;     for (int n = 0; n < quota; ++n) {
;         __syncthreads();
;         if (tid == 0) *slot = (int)atomicAdd(q, 1u);
;         __syncthreads();
;         const int t = *slot;
;         if (t >= DEF_GU + DEF_DN) break;
;         const bool gu = t < DEF_GU;
;         const float* src = gu ? P.in[34] : P.in[36]; bf16* dst = (bf16*)(P.ws + (gu ? WS_WGU : WS_WDN));
;         const int N = gu ? 2048 : 1024, ntn = N / 256, it = gu ? 2 * NE * 16 * 8 - DEF_GU + t : 2 * NE * 16 * 4 - DEF_DN + (t - DEF_GU);
; __global__ void __launch_bounds__(NT, 2) mega(Args args) {
;     ...
;         if (IDLE_LAST(68 * 7)) convert_deferred(P, lds, 4); } SEAM(2);
.LBB0_779:
	s_abs_i32 s3, s62
	v_cvt_f32_u32_e32 v2, s3
	s_sub_i32 s4, 0, s3
	s_mov_b32 s5, 0
	v_rcp_iflag_f32_e32 v2, v2
	s_nop 0
	v_mul_f32_e32 v2, 0x4f7ffffe, v2
	v_cvt_u32_f32_e32 v2, v2
	s_nop 0
	v_readfirstlane_b32 s6, v2
	s_mul_i32 s4, s4, s6
	s_mul_hi_u32 s4, s6, s4
	s_add_i32 s6, s6, s4
	s_mul_hi_u32 s4, s6, 0x1dc
	s_mul_i32 s4, s4, s3
	s_sub_i32 s4, 0x1dc, s4
	s_sub_i32 s6, s4, s3
	s_cmp_ge_u32 s4, s3
	s_cselect_b32 s4, s6, s4
	s_sub_i32 s6, s4, s3
	s_cmp_ge_u32 s4, s3
	s_cselect_b32 s3, s6, s4
	s_cmp_eq_u32 s3, 0
	s_cselect_b64 s[6:7], -1, 0
	s_cmp_lt_i32 s2, s3
	s_cselect_b64 s[8:9], -1, 0
	s_or_b64 s[6:7], s[6:7], s[8:9]
	s_and_b64 vcc, exec, s[6:7]
	s_cbranch_vccnz .LBB0_789
	v_and_b32_e32 v2, 0x7c, v155
	v_lshlrev_b32_e32 v3, 5, v0
	s_movk_i32 s3, 0x400
	v_lshrrev_b32_e32 v4, 6, v0
	v_and_or_b32 v12, v3, s3, v2
	v_bfe_u32 v2, v0, 3, 3
	v_lshl_or_b32 v5, v4, 5, v2
	v_lshlrev_b32_e32 v2, 3, v0
	v_lshl_add_u32 v11, v182, 4, 0
	v_and_b32_e32 v2, 56, v2
	v_mul_u32_u24_e32 v16, 0x2020, v4
	v_mov_b32_e32 v3, 0
	v_lshl_add_u32 v27, v5, 2, 0
	v_mul_u32_u24_e32 v28, 0x404, v2
	v_lshlrev_b32_e32 v10, 6, v5
	s_add_i32 s12, 0, 0x22c38
	v_add_u32_e32 v16, v11, v16
	v_and_b32_e32 v13, 0xfc, v155
	v_and_b32_e32 v14, 56, v154
	s_mov_b32 s3, 7
	s_mov_b32 s91, 0
	v_or_b32_e32 v4, 0x200, v10
	v_mov_b32_e32 v5, v3
	v_or_b32_e32 v6, 0x400, v10
	v_mov_b32_e32 v7, v3
	v_or_b32_e32 v8, 0x600, v10
	v_mov_b32_e32 v9, v3
	v_mov_b32_e32 v15, s12
	s_movk_i32 s13, 0x1517
	s_movk_i32 s14, 0x800
	s_mov_b32 s15, 0x1104e000
	s_movk_i32 s16, -1304
	v_add_u32_e32 v17, 0x404, v16
	v_add_u32_e32 v18, 0x40c, v16
	v_add_u32_e32 v19, 0x808, v16
	v_add_u32_e32 v20, 0xc0c, v16
	v_add_u32_e32 v21, 0xc14, v16
	v_add_u32_e32 v22, 0x1414, v16
	v_add_u32_e32 v23, 0x141c, v16
	v_add_u32_e32 v24, 0x1818, v16
	v_add_u32_e32 v25, 0x1c1c, v16
	v_add_u32_e32 v26, 0x1c24, v16
	v_lshlrev_b32_e32 v2, 1, v2
	v_add_u32_e32 v27, v27, v28
	v_lshlrev_b32_e32 v10, 1, v10
	s_branch .LBB0_782

; __device__ __forceinline__ unsigned g8_cvt_pk(float lo, float hi) { unsigned r; asm volatile("v_cvt_pk_bf16_f32 %0, %1, %2" : "=v"(r) : "v"(lo), "v"(hi)); return r; }
; __device__ __forceinline__ void convert_deferred(const Ptrs& P, unsigned char* lds, int quota) {
;     ...
;         const int t = *slot;
;         if (t >= DEF_GU + DEF_DN) break;
;         const bool gu = t < DEF_GU;
;         const float* src = gu ? P.in[34] : P.in[36]; bf16* dst = (bf16*)(P.ws + (gu ? WS_WGU : WS_WDN));
;         const int N = gu ? 2048 : 1024, ntn = N / 256, it = gu ? 2 * NE * 16 * 8 - DEF_GU + t : 2 * NE * 16 * 4 - DEF_DN + (t - DEF_GU);
;         f32x4 cur[8];
;         bt_load(src, N, gu ? 1 : 0, it, ntn, cur);
; #pragma unroll
;         for (int i = 0; i < 8; ++i) { float* tp = tile + (wid * 8 + i) * 257 + lane * 4; tp[0] = cur[i][0]; tp[1] = cur[i][1]; tp[2] = cur[i][2]; tp[3] = cur[i][3]; }
;         __syncthreads();
;         const int per = 16 * ntn, z = it / per, r = it % per, kt = r / ntn, nt = r % ntn;
;         bf16* d = dst + (size_t)z * N * 1024 + (((size_t)nt * 16 + kt) << 14);
;         const int kc = lane & 7;
; #pragma unroll
;         for (int pss = 0; pss < 4; ++pss) {
;             const int nn = wid * 32 + pss * 8 + (lane >> 3); float f[8];
; #pragma unroll
;             for (int j = 0; j < 8; ++j) f[j] = tile[(kc * 8 + j) * 257 + nn];
;             u32x4 w; w.x = g8_cvt_pk(f[0], f[1]); w.y = g8_cvt_pk(f[2], f[3]); w.z = g8_cvt_pk(f[4], f[5]); w.w = g8_cvt_pk(f[6], f[7]);
;             *(u32x4*)(d + nn * 64 + kc * 8) = w;
;         }
.LBB0_786:
	s_or_b64 exec, exec, s[6:7]
	s_waitcnt lgkmcnt(0)
	s_barrier
	ds_read_b32 v11, v15
	s_mov_b64 s[6:7], -1
	s_waitcnt lgkmcnt(0)
	v_cmp_lt_i32_e32 vcc, s13, v11
	v_readfirstlane_b32 s4, v11
	s_cbranch_vccnz .LBB0_781
	s_cmpk_gt_i32 s4, 0xe0f
	s_cselect_b64 vcc, -1, 0
	s_and_b64 s[6:7], vcc, exec
	s_cselect_b32 s6, s15, 0x104e000
	s_cselect_b32 s11, 0x400, s14
	s_cselect_b32 s17, s73, s69
	s_cselect_b32 s20, s72, s68
	s_cselect_b32 s7, s16, 0x11f0
	s_cselect_b32 s18, 20, 21
	s_cselect_b32 s21, 10, 11
	s_add_u32 s26, s78, s6
	s_addc_u32 s27, s79, 0
	s_lshr_b32 s8, s11, 4
	s_abs_i32 s6, s8
	v_cvt_f32_u32_e32 v11, s6
	s_sub_i32 s19, 0, s6
	s_add_i32 s7, s7, s4
	s_abs_i32 s9, s7
	v_rcp_iflag_f32_e32 v11, v11
	s_xor_b32 s4, s7, s8
	s_lshr_b32 s10, s11, 8
	s_ashr_i32 s4, s4, 31
	v_mul_f32_e32 v11, 0x4f7ffffe, v11
	v_cvt_u32_f32_e32 v11, v11
	s_nop 0
	v_readfirstlane_b32 s28, v11
	s_mul_i32 s19, s19, s28
	s_mul_hi_u32 s19, s28, s19
	s_add_i32 s28, s28, s19
	s_mul_hi_u32 s19, s9, s28
	s_mul_i32 s28, s19, s6
	s_sub_i32 s9, s9, s28
	s_add_i32 s28, s19, 1
	s_sub_i32 s29, s9, s6
	s_cmp_ge_u32 s9, s6
	s_cselect_b32 s19, s28, s19
	s_cselect_b32 s9, s29, s9
	s_add_i32 s28, s19, 1
	s_cmp_ge_u32 s9, s6
	s_cselect_b32 s6, s28, s19
	s_xor_b32 s6, s6, s4
	s_sub_i32 s6, s6, s4
	s_sext_i32_i8 s4, s10
	v_cvt_f32_i32_e32 v11, s4
	s_mul_i32 s8, s6, s8
	s_sub_i32 s7, s7, s8
	v_cvt_f32_i32_e32 v28, s7
	v_rcp_iflag_f32_e32 v29, v11
	s_xor_b32 s4, s7, s4
	s_ashr_i32 s4, s4, 30
	s_or_b32 s4, s4, 1
	v_mul_f32_e32 v29, v28, v29
	v_trunc_f32_e32 v29, v29
	v_fma_f32 v28, -v29, v11, v28
	v_cvt_i32_f32_e32 v29, v29
	v_cmp_ge_f32_e64 s[8:9], |v28|, |v11|
	s_and_b64 s[8:9], s[8:9], exec
	s_cselect_b32 s4, s4, 0
	v_readfirstlane_b32 s8, v29
	s_add_i32 s8, s8, s4
	s_mul_i32 s9, s8, s10
	s_sub_i32 s10, s7, s9
	s_sext_i32_i8 s7, s10
	v_lshl_add_u32 v11, s7, 7, v12
	v_lshl_or_b32 v28, s7, 8, v13
	s_ashr_i32 s7, s6, 31
	s_sext_i32_i8 s4, s8
	s_lshl_b64 s[18:19], s[6:7], s18
	v_lshl_or_b32 v30, s4, 6, v14
	s_lshl_b64 s[18:19], s[18:19], 2
	v_ashrrev_i32_e32 v31, 31, v30
	s_add_u32 s18, s20, s18
	v_cndmask_b32_e32 v28, v11, v28, vcc
	s_addc_u32 s19, s17, s19
	v_lshlrev_b64 v[30:31], s21, v[30:31]
	v_lshl_add_u64 v[30:31], v[30:31], 2, s[18:19]
	v_ashrrev_i32_e32 v29, 31, v28
	v_lshl_add_u64 v[52:53], v[28:29], 2, v[30:31]
	s_lshl_b64 s[18:19], 12, s21
	s_lshl_b32 s4, s11, 2
	v_lshl_add_u64 v[40:41], v[52:53], 0, s[18:19]
	s_lshl_b64 s[18:19], 24, s21
	v_lshl_add_u64 v[36:37], v[52:53], 0, s[4:5]
	v_lshl_add_u64 v[44:45], v[52:53], 0, s[18:19]
	s_lshl_b64 s[18:19], 28, s21
	v_lshl_add_u64 v[54:55], v[36:37], 0, s[4:5]
	v_lshl_add_u64 v[48:49], v[52:53], 0, s[18:19]
	s_lshl_b32 s4, s11, 3
	s_lshl_b64 s[18:19], 20, s21
	global_load_dwordx4 v[28:31], v[52:53], off nt
	global_load_dwordx4 v[32:35], v[36:37], off nt
	s_nop 0
	global_load_dwordx4 v[36:39], v[54:55], off nt
	s_nop 0
	global_load_dwordx4 v[40:43], v[40:41], off nt
	v_lshl_add_u64 v[54:55], v[54:55], 0, s[4:5]
	v_lshl_add_u64 v[56:57], v[52:53], 0, s[18:19]
	global_load_dwordx4 v[44:47], v[44:45], off nt
	s_nop 0
	global_load_dwordx4 v[48:51], v[48:49], off nt
	s_nop 0
	global_load_dwordx4 v[52:55], v[54:55], off nt
	s_nop 0
	global_load_dwordx4 v[56:59], v[56:57], off nt
	s_lshl_b64 s[6:7], s[6:7], s21
	s_lshl_b64 s[6:7], s[6:7], 11
	s_add_u32 s4, s26, s6
	s_addc_u32 s11, s27, s7
	s_bfe_i64 s[6:7], s[10:11], 0x80000
	s_bfe_i64 s[8:9], s[8:9], 0x80000
	s_lshl_b64 s[6:7], s[6:7], 19
	s_add_u32 s4, s4, s6
	s_addc_u32 s10, s11, s7
	s_lshl_b64 s[6:7], s[8:9], 15
	s_add_u32 s6, s4, s6
	s_addc_u32 s7, s10, s7
	v_mov_b32_e32 v11, v3
	s_add_i32 s3, s3, -1
	s_cmp_eq_u32 s3, 0
	s_waitcnt vmcnt(7)
	ds_write_b128 v16, v[28:31]
	s_waitcnt vmcnt(6)
	ds_write2_b32 v17, v32, v33 offset1:1
	ds_write2_b32 v18, v34, v35 offset1:1
	s_waitcnt vmcnt(3)
	ds_write2_b64 v24, v[44:45], v[46:47] offset1:1
	s_waitcnt vmcnt(2)
	ds_write2_b32 v25, v48, v49 offset1:1
	ds_write2_b32 v26, v50, v51 offset1:1
	ds_write2_b64 v19, v[36:37], v[38:39] offset1:1
	ds_write2_b32 v20, v40, v41 offset1:1
	ds_write2_b32 v21, v42, v43 offset1:1
	s_waitcnt vmcnt(1)
	ds_write_b128 v16, v[52:55] offset:4112
	s_waitcnt vmcnt(0)
	ds_write2_b32 v22, v56, v57 offset1:1
	ds_write2_b32 v23, v58, v59 offset1:1
	s_waitcnt lgkmcnt(0)
	s_barrier
	ds_read_b32 v28, v27 offset:1028
	ds_read_b32 v29, v27 offset:3084
	ds_read_b32 v30, v27 offset:5140
	ds_read_b32 v31, v27 offset:7196
	ds_read_b32 v32, v27 offset:6168
	ds_read_b32 v33, v27 offset:4112
	ds_read_b32 v34, v27 offset:2056
	ds_read_b32 v35, v27
	s_waitcnt lgkmcnt(0)
	v_cvt_pk_bf16_f32 v28, v35, v28
	v_cvt_pk_bf16_f32 v29, v34, v29
	v_cvt_pk_bf16_f32 v30, v33, v30
	v_cvt_pk_bf16_f32 v31, v32, v31
	ds_read_b32 v36, v27 offset:1060
	ds_read_b32 v37, v27 offset:3116
	ds_read_b32 v38, v27 offset:5172
	ds_read_b32 v39, v27 offset:7228
	ds_read_b32 v40, v27 offset:6200
	ds_read_b32 v41, v27 offset:4144
	ds_read_b32 v42, v27 offset:2088
	ds_read_b32 v43, v27 offset:32
	v_lshl_add_u64 v[32:33], s[6:7], 0, v[2:3]
	v_lshl_add_u64 v[34:35], v[32:33], 0, v[10:11]
	global_store_dwordx4 v[34:35], v[28:31], off
	v_lshl_add_u64 v[34:35], v[4:5], 1, v[32:33]
	s_cselect_b64 s[6:7], -1, 0
	s_waitcnt lgkmcnt(0)
	v_cvt_pk_bf16_f32 v28, v43, v36
	v_cvt_pk_bf16_f32 v29, v42, v37
	v_cvt_pk_bf16_f32 v30, v41, v38
	v_cvt_pk_bf16_f32 v31, v40, v39
	ds_read_b32 v11, v27 offset:1092
	ds_read_b32 v36, v27 offset:3148
	ds_read_b32 v37, v27 offset:6232
	ds_read_b32 v38, v27 offset:4176
	ds_read_b32 v39, v27 offset:2120
	ds_read_b32 v40, v27 offset:64
	ds_read_b32 v41, v27 offset:5204
	ds_read_b32 v42, v27 offset:7260
	global_store_dwordx4 v[34:35], v[28:31], off
	v_lshl_add_u64 v[34:35], v[6:7], 1, v[32:33]
	v_lshl_add_u64 v[32:33], v[8:9], 1, v[32:33]
	s_waitcnt lgkmcnt(2)
	v_cvt_pk_bf16_f32 v28, v40, v11
	v_cvt_pk_bf16_f32 v29, v39, v36
	s_waitcnt lgkmcnt(1)
	v_cvt_pk_bf16_f32 v30, v38, v41
	s_waitcnt lgkmcnt(0)
	v_cvt_pk_bf16_f32 v31, v37, v42
	ds_read_b32 v11, v27 offset:1124
	ds_read_b32 v36, v27 offset:3180
	ds_read_b32 v37, v27 offset:6264
	ds_read_b32 v38, v27 offset:4208
	ds_read_b32 v39, v27 offset:2152
	ds_read_b32 v40, v27 offset:96
	ds_read_b32 v41, v27 offset:5236
	ds_read_b32 v42, v27 offset:7292
	global_store_dwordx4 v[34:35], v[28:31], off
	s_waitcnt lgkmcnt(2)
	s_nop 0
	v_cvt_pk_bf16_f32 v28, v40, v11
	v_cvt_pk_bf16_f32 v29, v39, v36
	s_waitcnt lgkmcnt(1)
	v_cvt_pk_bf16_f32 v30, v38, v41
	s_waitcnt lgkmcnt(0)
	v_cvt_pk_bf16_f32 v31, v37, v42
	global_store_dwordx4 v[32:33], v[28:31], off
	s_branch .LBB0_781

; #define SEAM(k) do { if (IN(k) && IN((k) + 1)) xcd_barrier(bar); \
;         if (PROBE_MASK) { const unsigned long long t_ = __builtin_amdgcn_s_memrealtime(); if ((PROBE_MASK >> (k)) & 1u) pr_acc += t_ - pr_t0; pr_t0 = t_; } } while (0)
; __device__ __forceinline__ void convert_deferred(const Ptrs& P, unsigned char* lds, int quota) {
;     const int tid = threadIdx.x, wid = tid >> 6, lane = tid & 63;
;     float* tile = (float*)lds;
;     volatile __attribute__((address_space(3))) int* slot = (volatile __attribute__((address_space(3))) int*)((__attribute__((address_space(3))) unsigned char*)lds + 131072 + 320 + 11000);
;     unsigned* q = (unsigned*)(P.ws + WS_CTL) + CW_DEFQ;
;     for (int n = 0; n < quota; ++n) {
;         __syncthreads();
;         if (tid == 0) *slot = (int)atomicAdd(q, 1u);
;         __syncthreads();
;         const int t = *slot;
;         if (t >= DEF_GU + DEF_DN) break;
;         const bool gu = t < DEF_GU;
;         const float* src = gu ? P.in[34] : P.in[36]; bf16* dst = (bf16*)(P.ws + (gu ? WS_WGU : WS_WDN));
;         const int N = gu ? 2048 : 1024, ntn = N / 256, it = gu ? 2 * NE * 16 * 8 - DEF_GU + t : 2 * NE * 16 * 4 - DEF_DN + (t - DEF_GU);
; __global__ void __launch_bounds__(NT, 2) mega(Args args) {
;     ...
;         if (IDLE_LAST(68 * 4)) convert_deferred(P, lds, 4); } SEAM(6);
.LBB0_1286:
	s_abs_i32 s3, s62
	v_cvt_f32_u32_e32 v2, s3
	s_sub_i32 s4, 0, s3
	s_mov_b32 s5, 0
	v_rcp_iflag_f32_e32 v2, v2
	s_nop 0
	v_mul_f32_e32 v2, 0x4f7ffffe, v2
	v_cvt_u32_f32_e32 v2, v2
	s_nop 0
	v_readfirstlane_b32 s6, v2
	s_mul_i32 s4, s4, s6
	s_mul_hi_u32 s4, s6, s4
	s_add_i32 s6, s6, s4
	s_mul_hi_u32 s4, s6, 0x110
	s_mul_i32 s4, s4, s3
	s_sub_i32 s4, 0x110, s4
	s_sub_i32 s6, s4, s3
	s_cmp_ge_u32 s4, s3
	s_cselect_b32 s4, s6, s4
	s_sub_i32 s6, s4, s3
	s_cmp_ge_u32 s4, s3
	s_cselect_b32 s3, s6, s4
	s_cmp_eq_u32 s3, 0
	s_cselect_b64 s[6:7], -1, 0
	s_cmp_lt_i32 s2, s3
	s_cselect_b64 s[8:9], -1, 0
	s_or_b64 s[6:7], s[6:7], s[8:9]
	s_and_b64 vcc, exec, s[6:7]
	s_cbranch_vccnz .LBB0_1296
	v_and_b32_e32 v2, 0x7c, v188
	v_lshlrev_b32_e32 v3, 5, v0
	s_movk_i32 s3, 0x400
	v_and_or_b32 v12, v3, s3, v2
	v_bfe_u32 v2, v0, 3, 3
	v_lshl_or_b32 v4, v1, 5, v2
	v_lshlrev_b32_e32 v2, 3, v0
	v_lshl_add_u32 v11, v182, 4, 0
	v_and_b32_e32 v2, 56, v2
	v_mul_u32_u24_e32 v16, 0x2020, v1
	v_mov_b32_e32 v3, 0
	v_lshl_add_u32 v27, v4, 2, 0
	v_mul_u32_u24_e32 v28, 0x404, v2
	v_lshlrev_b32_e32 v10, 6, v4
	s_add_i32 s12, 0, 0x22c38
	v_add_u32_e32 v16, v11, v16
	v_and_b32_e32 v13, 0xfc, v188
	v_and_b32_e32 v14, 56, v185
	s_mov_b32 s3, 10
	s_mov_b32 s91, 0
	v_or_b32_e32 v4, 0x200, v10
	v_mov_b32_e32 v5, v3
	v_or_b32_e32 v6, 0x400, v10
	v_mov_b32_e32 v7, v3
	v_or_b32_e32 v8, 0x600, v10
	v_mov_b32_e32 v9, v3
	v_mov_b32_e32 v15, s12
	s_movk_i32 s13, 0x1517
	s_movk_i32 s14, 0x800
	s_mov_b32 s15, 0x1104e000
	s_movk_i32 s16, -1304
	v_add_u32_e32 v17, 0x404, v16
	v_add_u32_e32 v18, 0x40c, v16
	v_add_u32_e32 v19, 0x808, v16
	v_add_u32_e32 v20, 0xc0c, v16
	v_add_u32_e32 v21, 0xc14, v16
	v_add_u32_e32 v22, 0x1414, v16
	v_add_u32_e32 v23, 0x141c, v16
	v_add_u32_e32 v24, 0x1818, v16
	v_add_u32_e32 v25, 0x1c1c, v16
	v_add_u32_e32 v26, 0x1c24, v16
	v_lshlrev_b32_e32 v2, 1, v2
	v_add_u32_e32 v27, v27, v28
	v_lshlrev_b32_e32 v10, 1, v10
	s_branch .LBB0_1289

; __device__ __forceinline__ unsigned g8_cvt_pk(float lo, float hi) { unsigned r; asm volatile("v_cvt_pk_bf16_f32 %0, %1, %2" : "=v"(r) : "v"(lo), "v"(hi)); return r; }
; __device__ __forceinline__ void convert_deferred(const Ptrs& P, unsigned char* lds, int quota) {
;     ...
;         const int t = *slot;
;         if (t >= DEF_GU + DEF_DN) break;
;         const bool gu = t < DEF_GU;
;         const float* src = gu ? P.in[34] : P.in[36]; bf16* dst = (bf16*)(P.ws + (gu ? WS_WGU : WS_WDN));
;         const int N = gu ? 2048 : 1024, ntn = N / 256, it = gu ? 2 * NE * 16 * 8 - DEF_GU + t : 2 * NE * 16 * 4 - DEF_DN + (t - DEF_GU);
;         f32x4 cur[8];
;         bt_load(src, N, gu ? 1 : 0, it, ntn, cur);
; #pragma unroll
;         for (int i = 0; i < 8; ++i) { float* tp = tile + (wid * 8 + i) * 257 + lane * 4; tp[0] = cur[i][0]; tp[1] = cur[i][1]; tp[2] = cur[i][2]; tp[3] = cur[i][3]; }
;         __syncthreads();
;         const int per = 16 * ntn, z = it / per, r = it % per, kt = r / ntn, nt = r % ntn;
;         bf16* d = dst + (size_t)z * N * 1024 + (((size_t)nt * 16 + kt) << 14);
;         const int kc = lane & 7;
; #pragma unroll
;         for (int pss = 0; pss < 4; ++pss) {
;             const int nn = wid * 32 + pss * 8 + (lane >> 3); float f[8];
; #pragma unroll
;             for (int j = 0; j < 8; ++j) f[j] = tile[(kc * 8 + j) * 257 + nn];
;             u32x4 w; w.x = g8_cvt_pk(f[0], f[1]); w.y = g8_cvt_pk(f[2], f[3]); w.z = g8_cvt_pk(f[4], f[5]); w.w = g8_cvt_pk(f[6], f[7]);
;             *(u32x4*)(d + nn * 64 + kc * 8) = w;
;         }
.LBB0_1293:
	s_or_b64 exec, exec, s[6:7]
	s_waitcnt lgkmcnt(0)
	s_barrier
	ds_read_b32 v11, v15
	s_mov_b64 s[6:7], -1
	s_waitcnt lgkmcnt(0)
	v_cmp_lt_i32_e32 vcc, s13, v11
	v_readfirstlane_b32 s4, v11
	s_cbranch_vccnz .LBB0_1288
	s_cmpk_gt_i32 s4, 0xe0f
	s_cselect_b64 vcc, -1, 0
	s_and_b64 s[6:7], vcc, exec
	s_cselect_b32 s6, s15, 0x104e000
	s_cselect_b32 s11, 0x400, s14
	s_cselect_b32 s17, s73, s69
	s_cselect_b32 s20, s72, s68
	s_cselect_b32 s7, s16, 0x11f0
	s_cselect_b32 s18, 20, 21
	s_cselect_b32 s21, 10, 11
	s_add_u32 s22, s78, s6
	s_addc_u32 s23, s79, 0
	s_lshr_b32 s8, s11, 4
	s_abs_i32 s6, s8
	v_cvt_f32_u32_e32 v11, s6
	s_sub_i32 s19, 0, s6
	s_add_i32 s7, s7, s4
	s_abs_i32 s9, s7
	v_rcp_iflag_f32_e32 v11, v11
	s_xor_b32 s4, s7, s8
	s_lshr_b32 s10, s11, 8
	s_ashr_i32 s4, s4, 31
	v_mul_f32_e32 v11, 0x4f7ffffe, v11
	v_cvt_u32_f32_e32 v11, v11
	s_nop 0
	v_readfirstlane_b32 s24, v11
	s_mul_i32 s19, s19, s24
	s_mul_hi_u32 s19, s24, s19
	s_add_i32 s24, s24, s19
	s_mul_hi_u32 s19, s9, s24
	s_mul_i32 s24, s19, s6
	s_sub_i32 s9, s9, s24
	s_add_i32 s24, s19, 1
	s_sub_i32 s25, s9, s6
	s_cmp_ge_u32 s9, s6
	s_cselect_b32 s19, s24, s19
	s_cselect_b32 s9, s25, s9
	s_add_i32 s24, s19, 1
	s_cmp_ge_u32 s9, s6
	s_cselect_b32 s6, s24, s19
	s_xor_b32 s6, s6, s4
	s_sub_i32 s6, s6, s4
	s_sext_i32_i8 s4, s10
	v_cvt_f32_i32_e32 v11, s4
	s_mul_i32 s8, s6, s8
	s_sub_i32 s7, s7, s8
	v_cvt_f32_i32_e32 v28, s7
	v_rcp_iflag_f32_e32 v29, v11
	s_xor_b32 s4, s7, s4
	s_ashr_i32 s4, s4, 30
	s_or_b32 s4, s4, 1
	v_mul_f32_e32 v29, v28, v29
	v_trunc_f32_e32 v29, v29
	v_fma_f32 v28, -v29, v11, v28
	v_cvt_i32_f32_e32 v29, v29
	v_cmp_ge_f32_e64 s[8:9], |v28|, |v11|
	s_and_b64 s[8:9], s[8:9], exec
	s_cselect_b32 s4, s4, 0
	v_readfirstlane_b32 s8, v29
	s_add_i32 s8, s8, s4
	s_mul_i32 s9, s8, s10
	s_sub_i32 s10, s7, s9
	s_sext_i32_i8 s7, s10
	v_lshl_add_u32 v11, s7, 7, v12
	v_lshl_or_b32 v28, s7, 8, v13
	s_ashr_i32 s7, s6, 31
	s_sext_i32_i8 s4, s8
	s_lshl_b64 s[18:19], s[6:7], s18
	v_lshl_or_b32 v30, s4, 6, v14
	s_lshl_b64 s[18:19], s[18:19], 2
	v_ashrrev_i32_e32 v31, 31, v30
	s_add_u32 s18, s20, s18
	v_cndmask_b32_e32 v28, v11, v28, vcc
	s_addc_u32 s19, s17, s19
	v_lshlrev_b64 v[30:31], s21, v[30:31]
	v_lshl_add_u64 v[30:31], v[30:31], 2, s[18:19]
	v_ashrrev_i32_e32 v29, 31, v28
	v_lshl_add_u64 v[52:53], v[28:29], 2, v[30:31]
	s_lshl_b64 s[18:19], 12, s21
	s_lshl_b32 s4, s11, 2
	v_lshl_add_u64 v[40:41], v[52:53], 0, s[18:19]
	s_lshl_b64 s[18:19], 24, s21
	v_lshl_add_u64 v[36:37], v[52:53], 0, s[4:5]
	v_lshl_add_u64 v[44:45], v[52:53], 0, s[18:19]
	s_lshl_b64 s[18:19], 28, s21
	v_lshl_add_u64 v[54:55], v[36:37], 0, s[4:5]
	v_lshl_add_u64 v[48:49], v[52:53], 0, s[18:19]
	s_lshl_b32 s4, s11, 3
	s_lshl_b64 s[18:19], 20, s21
	global_load_dwordx4 v[28:31], v[52:53], off nt
	global_load_dwordx4 v[32:35], v[36:37], off nt
	s_nop 0
	global_load_dwordx4 v[36:39], v[54:55], off nt
	s_nop 0
	global_load_dwordx4 v[40:43], v[40:41], off nt
	v_lshl_add_u64 v[54:55], v[54:55], 0, s[4:5]
	v_lshl_add_u64 v[56:57], v[52:53], 0, s[18:19]
	global_load_dwordx4 v[44:47], v[44:45], off nt
	s_nop 0
	global_load_dwordx4 v[48:51], v[48:49], off nt
	s_nop 0
	global_load_dwordx4 v[52:55], v[54:55], off nt
	s_nop 0
	global_load_dwordx4 v[56:59], v[56:57], off nt
	s_lshl_b64 s[6:7], s[6:7], s21
	s_lshl_b64 s[6:7], s[6:7], 11
	s_add_u32 s4, s22, s6
	s_addc_u32 s11, s23, s7
	s_bfe_i64 s[6:7], s[10:11], 0x80000
	s_bfe_i64 s[8:9], s[8:9], 0x80000
	s_lshl_b64 s[6:7], s[6:7], 19
	s_add_u32 s4, s4, s6
	s_addc_u32 s10, s11, s7
	s_lshl_b64 s[6:7], s[8:9], 15
	s_add_u32 s6, s4, s6
	s_addc_u32 s7, s10, s7
	v_mov_b32_e32 v11, v3
	s_add_i32 s3, s3, -1
	s_cmp_eq_u32 s3, 0
	s_waitcnt vmcnt(7)
	ds_write_b128 v16, v[28:31]
	s_waitcnt vmcnt(6)
	ds_write2_b32 v17, v32, v33 offset1:1
	ds_write2_b32 v18, v34, v35 offset1:1
	s_waitcnt vmcnt(3)
	ds_write2_b64 v24, v[44:45], v[46:47] offset1:1
	s_waitcnt vmcnt(2)
	ds_write2_b32 v25, v48, v49 offset1:1
	ds_write2_b32 v26, v50, v51 offset1:1
	ds_write2_b64 v19, v[36:37], v[38:39] offset1:1
	ds_write2_b32 v20, v40, v41 offset1:1
	ds_write2_b32 v21, v42, v43 offset1:1
	s_waitcnt vmcnt(1)
	ds_write_b128 v16, v[52:55] offset:4112
	s_waitcnt vmcnt(0)
	ds_write2_b32 v22, v56, v57 offset1:1
	ds_write2_b32 v23, v58, v59 offset1:1
	s_waitcnt lgkmcnt(0)
	s_barrier
	ds_read_b32 v28, v27 offset:1028
	ds_read_b32 v29, v27 offset:3084
	ds_read_b32 v30, v27 offset:5140
	ds_read_b32 v31, v27 offset:7196
	ds_read_b32 v32, v27 offset:6168
	ds_read_b32 v33, v27 offset:4112
	ds_read_b32 v34, v27 offset:2056
	ds_read_b32 v35, v27
	s_waitcnt lgkmcnt(0)
	v_cvt_pk_bf16_f32 v28, v35, v28
	v_cvt_pk_bf16_f32 v29, v34, v29
	v_cvt_pk_bf16_f32 v30, v33, v30
	v_cvt_pk_bf16_f32 v31, v32, v31
	ds_read_b32 v36, v27 offset:1060
	ds_read_b32 v37, v27 offset:3116
	ds_read_b32 v38, v27 offset:5172
	ds_read_b32 v39, v27 offset:7228
	ds_read_b32 v40, v27 offset:6200
	ds_read_b32 v41, v27 offset:4144
	ds_read_b32 v42, v27 offset:2088
	ds_read_b32 v43, v27 offset:32
	v_lshl_add_u64 v[32:33], s[6:7], 0, v[2:3]
	v_lshl_add_u64 v[34:35], v[32:33], 0, v[10:11]
	global_store_dwordx4 v[34:35], v[28:31], off
	v_lshl_add_u64 v[34:35], v[4:5], 1, v[32:33]
	s_cselect_b64 s[6:7], -1, 0
	s_waitcnt lgkmcnt(0)
	v_cvt_pk_bf16_f32 v28, v43, v36
	v_cvt_pk_bf16_f32 v29, v42, v37
	v_cvt_pk_bf16_f32 v30, v41, v38
	v_cvt_pk_bf16_f32 v31, v40, v39
	ds_read_b32 v11, v27 offset:1092
	ds_read_b32 v36, v27 offset:3148
	ds_read_b32 v37, v27 offset:6232
	ds_read_b32 v38, v27 offset:4176
	ds_read_b32 v39, v27 offset:2120
	ds_read_b32 v40, v27 offset:64
	ds_read_b32 v41, v27 offset:5204
	ds_read_b32 v42, v27 offset:7260
	global_store_dwordx4 v[34:35], v[28:31], off
	v_lshl_add_u64 v[34:35], v[6:7], 1, v[32:33]
	v_lshl_add_u64 v[32:33], v[8:9], 1, v[32:33]
	s_waitcnt lgkmcnt(2)
	v_cvt_pk_bf16_f32 v28, v40, v11
	v_cvt_pk_bf16_f32 v29, v39, v36
	s_waitcnt lgkmcnt(1)
	v_cvt_pk_bf16_f32 v30, v38, v41
	s_waitcnt lgkmcnt(0)
	v_cvt_pk_bf16_f32 v31, v37, v42
	ds_read_b32 v11, v27 offset:1124
	ds_read_b32 v36, v27 offset:3180
	ds_read_b32 v37, v27 offset:6264
	ds_read_b32 v38, v27 offset:4208
	ds_read_b32 v39, v27 offset:2152
	ds_read_b32 v40, v27 offset:96
	ds_read_b32 v41, v27 offset:5236
	ds_read_b32 v42, v27 offset:7292
	global_store_dwordx4 v[34:35], v[28:31], off
	s_waitcnt lgkmcnt(2)
	s_nop 0
	v_cvt_pk_bf16_f32 v28, v40, v11
	v_cvt_pk_bf16_f32 v29, v39, v36
	s_waitcnt lgkmcnt(1)
	v_cvt_pk_bf16_f32 v30, v38, v41
	s_waitcnt lgkmcnt(0)
	v_cvt_pk_bf16_f32 v31, v37, v42
	global_store_dwordx4 v[32:33], v[28:31], off
	s_branch .LBB0_1288

; #define LAS __attribute__((address_space(3)))
; #define SEAM(k) do { if (IN(k) && IN((k) + 1)) xcd_barrier(bar); \
;         if (PROBE_MASK) { const unsigned long long t_ = __builtin_amdgcn_s_memrealtime(); if ((PROBE_MASK >> (k)) & 1u) pr_acc += t_ - pr_t0; pr_t0 = t_; } } while (0)
; __device__ __forceinline__ void convert_deferred(const Ptrs& P, unsigned char* lds, int quota) {
;     const int tid = threadIdx.x, wid = tid >> 6, lane = tid & 63;
;     float* tile = (float*)lds;
;     volatile __attribute__((address_space(3))) int* slot = (volatile __attribute__((address_space(3))) int*)((__attribute__((address_space(3))) unsigned char*)lds + 131072 + 320 + 11000);
;     unsigned* q = (unsigned*)(P.ws + WS_CTL) + CW_DEFQ;
;     for (int n = 0; n < quota; ++n) {
;         __syncthreads();
;         if (tid == 0) *slot = (int)atomicAdd(q, 1u);
;         __syncthreads();
;         const int t = *slot;
;         if (t >= DEF_GU + DEF_DN) break;
;         const bool gu = t < DEF_GU;
;         const float* src = gu ? P.in[34] : P.in[36]; bf16* dst = (bf16*)(P.ws + (gu ? WS_WGU : WS_WDN));
;         const int N = gu ? 2048 : 1024, ntn = N / 256, it = gu ? 2 * NE * 16 * 8 - DEF_GU + t : 2 * NE * 16 * 4 - DEF_DN + (t - DEF_GU);
; __global__ void __launch_bounds__(NT, 2) mega(Args args) {
;     ...
;         { const int rem_ = ((LAS int*)(LDSP + MISC_OFF + 256))[96] % G; if (rem_ != 0 && vcu >= rem_) convert_deferred(P, lds, 5); } } SEAM(9);
.LBB0_1609:
	s_abs_i32 s0, s62
	v_cvt_f32_u32_e32 v2, s0
	s_sub_i32 s5, 0, s0
	s_abs_i32 s4, s9
	s_ashr_i32 s3, s9, 31
	v_rcp_iflag_f32_e32 v2, v2
	s_mov_b32 s1, 0
	v_mul_f32_e32 v2, 0x4f7ffffe, v2
	v_cvt_u32_f32_e32 v2, v2
	s_nop 0
	v_readfirstlane_b32 s6, v2
	s_mul_i32 s5, s5, s6
	s_mul_hi_u32 s5, s6, s5
	s_add_i32 s6, s6, s5
	s_mul_hi_u32 s5, s4, s6
	s_mul_i32 s5, s5, s0
	s_sub_i32 s4, s4, s5
	s_sub_i32 s5, s4, s0
	s_cmp_ge_u32 s4, s0
	s_cselect_b32 s4, s5, s4
	s_sub_i32 s5, s4, s0
	s_cmp_ge_u32 s4, s0
	s_cselect_b32 s0, s5, s4
	s_xor_b32 s0, s0, s3
	s_sub_i32 s0, s0, s3
	s_cmp_eq_u32 s0, 0
	v_readlane_b32 s3, v254, 2
	s_cselect_b64 s[4:5], -1, 0
	s_cmp_lt_i32 s3, s0
	s_cselect_b64 s[6:7], -1, 0
	s_or_b64 s[4:5], s[4:5], s[6:7]
	s_and_b64 vcc, exec, s[4:5]
	s_cbranch_vccnz .LBB0_1619
	v_and_b32_e32 v2, 0x7c, v175
	v_lshlrev_b32_e32 v3, 5, v0
	s_movk_i32 s0, 0x400
	v_and_or_b32 v12, v3, s0, v2
	v_bfe_u32 v2, v0, 3, 3
	v_lshl_or_b32 v4, v1, 5, v2
	v_lshlrev_b32_e32 v2, 3, v0
	v_lshl_add_u32 v11, v182, 4, 0
	v_and_b32_e32 v2, 56, v2
	v_mul_u32_u24_e32 v16, 0x2020, v1
	v_mov_b32_e32 v3, 0
	v_lshl_add_u32 v27, v4, 2, 0
	v_mul_u32_u24_e32 v28, 0x404, v2
	v_lshlrev_b32_e32 v10, 6, v4
	s_add_i32 s10, 0, 0x22c38
	v_add_u32_e32 v16, v11, v16
	s_mov_b32 s3, 9
	s_mov_b32 s91, 0
	v_and_b32_e32 v13, 0xfc, v175
	v_and_b32_e32 v14, 56, v173
	v_or_b32_e32 v4, 0x200, v10
	v_mov_b32_e32 v5, v3
	v_or_b32_e32 v6, 0x400, v10
	v_mov_b32_e32 v7, v3
	v_or_b32_e32 v8, 0x600, v10
	v_mov_b32_e32 v9, v3
	v_mov_b32_e32 v15, s10
	s_movk_i32 s11, 0x1517
	s_movk_i32 s12, 0x800
	s_mov_b32 s13, 0x1104e000
	s_movk_i32 s14, -1304
	v_add_u32_e32 v17, 0x404, v16
	v_add_u32_e32 v18, 0x40c, v16
	v_add_u32_e32 v19, 0x808, v16
	v_add_u32_e32 v20, 0xc0c, v16
	v_add_u32_e32 v21, 0xc14, v16
	v_add_u32_e32 v22, 0x1414, v16
	v_add_u32_e32 v23, 0x141c, v16
	v_add_u32_e32 v24, 0x1818, v16
	v_add_u32_e32 v25, 0x1c1c, v16
	v_add_u32_e32 v26, 0x1c24, v16
	v_lshlrev_b32_e32 v2, 1, v2
	v_add_u32_e32 v27, v27, v28
	v_lshlrev_b32_e32 v10, 1, v10
	s_branch .LBB0_1612

; __device__ __forceinline__ unsigned g8_cvt_pk(float lo, float hi) { unsigned r; asm volatile("v_cvt_pk_bf16_f32 %0, %1, %2" : "=v"(r) : "v"(lo), "v"(hi)); return r; }
; __device__ __forceinline__ void convert_deferred(const Ptrs& P, unsigned char* lds, int quota) {
;     ...
;         const int t = *slot;
;         if (t >= DEF_GU + DEF_DN) break;
;         const bool gu = t < DEF_GU;
;         const float* src = gu ? P.in[34] : P.in[36]; bf16* dst = (bf16*)(P.ws + (gu ? WS_WGU : WS_WDN));
;         const int N = gu ? 2048 : 1024, ntn = N / 256, it = gu ? 2 * NE * 16 * 8 - DEF_GU + t : 2 * NE * 16 * 4 - DEF_DN + (t - DEF_GU);
;         f32x4 cur[8];
;         bt_load(src, N, gu ? 1 : 0, it, ntn, cur);
; #pragma unroll
;         for (int i = 0; i < 8; ++i) { float* tp = tile + (wid * 8 + i) * 257 + lane * 4; tp[0] = cur[i][0]; tp[1] = cur[i][1]; tp[2] = cur[i][2]; tp[3] = cur[i][3]; }
;         __syncthreads();
;         const int per = 16 * ntn, z = it / per, r = it % per, kt = r / ntn, nt = r % ntn;
;         bf16* d = dst + (size_t)z * N * 1024 + (((size_t)nt * 16 + kt) << 14);
;         const int kc = lane & 7;
; #pragma unroll
;         for (int pss = 0; pss < 4; ++pss) {
;             const int nn = wid * 32 + pss * 8 + (lane >> 3); float f[8];
; #pragma unroll
;             for (int j = 0; j < 8; ++j) f[j] = tile[(kc * 8 + j) * 257 + nn];
;             u32x4 w; w.x = g8_cvt_pk(f[0], f[1]); w.y = g8_cvt_pk(f[2], f[3]); w.z = g8_cvt_pk(f[4], f[5]); w.w = g8_cvt_pk(f[6], f[7]);
;             *(u32x4*)(d + nn * 64 + kc * 8) = w;
;         }
.LBB0_1616:
	s_or_b64 exec, exec, s[4:5]
	s_waitcnt lgkmcnt(0)
	s_barrier
	ds_read_b32 v11, v15
	s_mov_b64 s[4:5], -1
	s_waitcnt lgkmcnt(0)
	v_cmp_lt_i32_e32 vcc, s11, v11
	v_readfirstlane_b32 s0, v11
	s_cbranch_vccnz .LBB0_1611
	s_cmpk_gt_i32 s0, 0xe0f
	s_cselect_b64 vcc, -1, 0
	s_and_b64 s[4:5], vcc, exec
	s_cselect_b32 s4, s13, 0x104e000
	s_cselect_b32 s9, 0x400, s12
	s_cselect_b32 s15, s73, s69
	s_cselect_b32 s18, s72, s68
	s_cselect_b32 s5, s14, 0x11f0
	s_cselect_b32 s16, 20, 21
	s_cselect_b32 s19, 10, 11
	s_add_u32 s20, s78, s4
	s_addc_u32 s21, s79, 0
	s_lshr_b32 s6, s9, 4
	s_abs_i32 s4, s6
	v_cvt_f32_u32_e32 v11, s4
	s_sub_i32 s17, 0, s4
	s_add_i32 s5, s5, s0
	s_abs_i32 s7, s5
	v_rcp_iflag_f32_e32 v11, v11
	s_xor_b32 s0, s5, s6
	s_lshr_b32 s8, s9, 8
	s_ashr_i32 s0, s0, 31
	v_mul_f32_e32 v11, 0x4f7ffffe, v11
	v_cvt_u32_f32_e32 v11, v11
	s_nop 0
	v_readfirstlane_b32 s22, v11
	s_mul_i32 s17, s17, s22
	s_mul_hi_u32 s17, s22, s17
	s_add_i32 s22, s22, s17
	s_mul_hi_u32 s17, s7, s22
	s_mul_i32 s22, s17, s4
	s_sub_i32 s7, s7, s22
	s_add_i32 s22, s17, 1
	s_sub_i32 s23, s7, s4
	s_cmp_ge_u32 s7, s4
	s_cselect_b32 s17, s22, s17
	s_cselect_b32 s7, s23, s7
	s_add_i32 s22, s17, 1
	s_cmp_ge_u32 s7, s4
	s_cselect_b32 s4, s22, s17
	s_xor_b32 s4, s4, s0
	s_sub_i32 s4, s4, s0
	s_sext_i32_i8 s0, s8
	v_cvt_f32_i32_e32 v11, s0
	s_mul_i32 s6, s4, s6
	s_sub_i32 s5, s5, s6
	v_cvt_f32_i32_e32 v28, s5
	v_rcp_iflag_f32_e32 v29, v11
	s_xor_b32 s0, s5, s0
	s_ashr_i32 s0, s0, 30
	s_or_b32 s0, s0, 1
	v_mul_f32_e32 v29, v28, v29
	v_trunc_f32_e32 v29, v29
	v_fma_f32 v28, -v29, v11, v28
	v_cvt_i32_f32_e32 v29, v29
	v_cmp_ge_f32_e64 s[6:7], |v28|, |v11|
	s_and_b64 s[6:7], s[6:7], exec
	s_cselect_b32 s0, s0, 0
	v_readfirstlane_b32 s6, v29
	s_add_i32 s6, s6, s0
	s_mul_i32 s7, s6, s8
	s_sub_i32 s8, s5, s7
	s_sext_i32_i8 s5, s8
	v_lshl_add_u32 v11, s5, 7, v12
	v_lshl_or_b32 v28, s5, 8, v13
	s_ashr_i32 s5, s4, 31
	s_sext_i32_i8 s0, s6
	s_lshl_b64 s[16:17], s[4:5], s16
	v_lshl_or_b32 v30, s0, 6, v14
	s_lshl_b64 s[16:17], s[16:17], 2
	v_ashrrev_i32_e32 v31, 31, v30
	s_add_u32 s16, s18, s16
	v_cndmask_b32_e32 v28, v11, v28, vcc
	s_addc_u32 s17, s15, s17
	v_lshlrev_b64 v[30:31], s19, v[30:31]
	v_lshl_add_u64 v[30:31], v[30:31], 2, s[16:17]
	v_ashrrev_i32_e32 v29, 31, v28
	v_lshl_add_u64 v[52:53], v[28:29], 2, v[30:31]
	s_lshl_b64 s[16:17], 12, s19
	s_lshl_b32 s0, s9, 2
	v_lshl_add_u64 v[40:41], v[52:53], 0, s[16:17]
	s_lshl_b64 s[16:17], 24, s19
	v_lshl_add_u64 v[36:37], v[52:53], 0, s[0:1]
	v_lshl_add_u64 v[44:45], v[52:53], 0, s[16:17]
	s_lshl_b64 s[16:17], 28, s19
	v_lshl_add_u64 v[54:55], v[36:37], 0, s[0:1]
	v_lshl_add_u64 v[48:49], v[52:53], 0, s[16:17]
	s_lshl_b32 s0, s9, 3
	s_lshl_b64 s[16:17], 20, s19
	global_load_dwordx4 v[28:31], v[52:53], off nt
	global_load_dwordx4 v[32:35], v[36:37], off nt
	s_nop 0
	global_load_dwordx4 v[36:39], v[54:55], off nt
	s_nop 0
	global_load_dwordx4 v[40:43], v[40:41], off nt
	v_lshl_add_u64 v[54:55], v[54:55], 0, s[0:1]
	v_lshl_add_u64 v[56:57], v[52:53], 0, s[16:17]
	global_load_dwordx4 v[44:47], v[44:45], off nt
	s_nop 0
	global_load_dwordx4 v[48:51], v[48:49], off nt
	s_nop 0
	global_load_dwordx4 v[52:55], v[54:55], off nt
	s_nop 0
	global_load_dwordx4 v[56:59], v[56:57], off nt
	s_lshl_b64 s[4:5], s[4:5], s19
	s_lshl_b64 s[4:5], s[4:5], 11
	s_add_u32 s0, s20, s4
	s_addc_u32 s9, s21, s5
	s_bfe_i64 s[4:5], s[8:9], 0x80000
	s_bfe_i64 s[6:7], s[6:7], 0x80000
	s_lshl_b64 s[4:5], s[4:5], 19
	s_add_u32 s0, s0, s4
	s_addc_u32 s8, s9, s5
	s_lshl_b64 s[4:5], s[6:7], 15
	s_add_u32 s4, s0, s4
	s_addc_u32 s5, s8, s5
	v_mov_b32_e32 v11, v3
	s_add_i32 s3, s3, -1
	s_cmp_eq_u32 s3, 0
	s_waitcnt vmcnt(7)
	ds_write_b128 v16, v[28:31]
	s_waitcnt vmcnt(6)
	ds_write2_b32 v17, v32, v33 offset1:1
	ds_write2_b32 v18, v34, v35 offset1:1
	s_waitcnt vmcnt(3)
	ds_write2_b64 v24, v[44:45], v[46:47] offset1:1
	s_waitcnt vmcnt(2)
	ds_write2_b32 v25, v48, v49 offset1:1
	ds_write2_b32 v26, v50, v51 offset1:1
	ds_write2_b64 v19, v[36:37], v[38:39] offset1:1
	ds_write2_b32 v20, v40, v41 offset1:1
	ds_write2_b32 v21, v42, v43 offset1:1
	s_waitcnt vmcnt(1)
	ds_write_b128 v16, v[52:55] offset:4112
	s_waitcnt vmcnt(0)
	ds_write2_b32 v22, v56, v57 offset1:1
	ds_write2_b32 v23, v58, v59 offset1:1
	s_waitcnt lgkmcnt(0)
	s_barrier
	ds_read_b32 v28, v27 offset:1028
	ds_read_b32 v29, v27 offset:3084
	ds_read_b32 v30, v27 offset:5140
	ds_read_b32 v31, v27 offset:7196
	ds_read_b32 v32, v27 offset:6168
	ds_read_b32 v33, v27 offset:4112
	ds_read_b32 v34, v27 offset:2056
	ds_read_b32 v35, v27
	s_waitcnt lgkmcnt(0)
	v_cvt_pk_bf16_f32 v28, v35, v28
	v_cvt_pk_bf16_f32 v29, v34, v29
	v_cvt_pk_bf16_f32 v30, v33, v30
	v_cvt_pk_bf16_f32 v31, v32, v31
	ds_read_b32 v36, v27 offset:1060
	ds_read_b32 v37, v27 offset:3116
	ds_read_b32 v38, v27 offset:5172
	ds_read_b32 v39, v27 offset:7228
	ds_read_b32 v40, v27 offset:6200
	ds_read_b32 v41, v27 offset:4144
	ds_read_b32 v42, v27 offset:2088
	ds_read_b32 v43, v27 offset:32
	v_lshl_add_u64 v[32:33], s[4:5], 0, v[2:3]
	v_lshl_add_u64 v[34:35], v[32:33], 0, v[10:11]
	global_store_dwordx4 v[34:35], v[28:31], off
	v_lshl_add_u64 v[34:35], v[4:5], 1, v[32:33]
	s_cselect_b64 s[4:5], -1, 0
	s_waitcnt lgkmcnt(0)
	v_cvt_pk_bf16_f32 v28, v43, v36
	v_cvt_pk_bf16_f32 v29, v42, v37
	v_cvt_pk_bf16_f32 v30, v41, v38
	v_cvt_pk_bf16_f32 v31, v40, v39
	ds_read_b32 v11, v27 offset:1092
	ds_read_b32 v36, v27 offset:3148
	ds_read_b32 v37, v27 offset:6232
	ds_read_b32 v38, v27 offset:4176
	ds_read_b32 v39, v27 offset:2120
	ds_read_b32 v40, v27 offset:64
	ds_read_b32 v41, v27 offset:5204
	ds_read_b32 v42, v27 offset:7260
	global_store_dwordx4 v[34:35], v[28:31], off
	v_lshl_add_u64 v[34:35], v[6:7], 1, v[32:33]
	v_lshl_add_u64 v[32:33], v[8:9], 1, v[32:33]
	s_waitcnt lgkmcnt(2)
	v_cvt_pk_bf16_f32 v28, v40, v11
	v_cvt_pk_bf16_f32 v29, v39, v36
	s_waitcnt lgkmcnt(1)
	v_cvt_pk_bf16_f32 v30, v38, v41
	s_waitcnt lgkmcnt(0)
	v_cvt_pk_bf16_f32 v31, v37, v42
	ds_read_b32 v11, v27 offset:1124
	ds_read_b32 v36, v27 offset:3180
	ds_read_b32 v37, v27 offset:6264
	ds_read_b32 v38, v27 offset:4208
	ds_read_b32 v39, v27 offset:2152
	ds_read_b32 v40, v27 offset:96
	ds_read_b32 v41, v27 offset:5236
	ds_read_b32 v42, v27 offset:7292
	global_store_dwordx4 v[34:35], v[28:31], off
	s_waitcnt lgkmcnt(2)
	s_nop 0
	v_cvt_pk_bf16_f32 v28, v40, v11
	v_cvt_pk_bf16_f32 v29, v39, v36
	s_waitcnt lgkmcnt(1)
	v_cvt_pk_bf16_f32 v30, v38, v41
	s_waitcnt lgkmcnt(0)
	v_cvt_pk_bf16_f32 v31, v37, v42
	global_store_dwordx4 v[32:33], v[28:31], off
	s_branch .LBB0_1611

; #define SEAM(k) do { if (IN(k) && IN((k) + 1)) xcd_barrier(bar); \
;         if (PROBE_MASK) { const unsigned long long t_ = __builtin_amdgcn_s_memrealtime(); if ((PROBE_MASK >> (k)) & 1u) pr_acc += t_ - pr_t0; pr_t0 = t_; } } while (0)
; __device__ __forceinline__ void convert_deferred(const Ptrs& P, unsigned char* lds, int quota) {
;     const int tid = threadIdx.x, wid = tid >> 6, lane = tid & 63;
;     float* tile = (float*)lds;
;     volatile __attribute__((address_space(3))) int* slot = (volatile __attribute__((address_space(3))) int*)((__attribute__((address_space(3))) unsigned char*)lds + 131072 + 320 + 11000);
;     unsigned* q = (unsigned*)(P.ws + WS_CTL) + CW_DEFQ;
;     for (int n = 0; n < quota; ++n) {
;         __syncthreads();
;         if (tid == 0) *slot = (int)atomicAdd(q, 1u);
;         __syncthreads();
;         const int t = *slot;
;         if (t >= DEF_GU + DEF_DN) break;
;         const bool gu = t < DEF_GU;
;         const float* src = gu ? P.in[34] : P.in[36]; bf16* dst = (bf16*)(P.ws + (gu ? WS_WGU : WS_WDN));
;         const int N = gu ? 2048 : 1024, ntn = N / 256, it = gu ? 2 * NE * 16 * 8 - DEF_GU + t : 2 * NE * 16 * 4 - DEF_DN + (t - DEF_GU);
; __global__ void __launch_bounds__(NT, 2) mega(Args args) {
;     ...
;         if (IDLE_LAST(68 * 12)) convert_deferred(P, lds, 4); } SEAM(11);
.LBB0_1851:
	s_abs_i32 s0, s62
	v_cvt_f32_u32_e32 v2, s0
	s_sub_i32 s3, 0, s0
	v_readlane_b32 s56, v254, 40
	s_mov_b32 s1, 0
	v_rcp_iflag_f32_e32 v2, v2
	v_readlane_b32 s57, v254, 41
	v_mul_f32_e32 v2, 0x4f7ffffe, v2
	v_cvt_u32_f32_e32 v2, v2
	s_nop 0
	v_readfirstlane_b32 s4, v2
	s_mul_i32 s3, s3, s4
	s_mul_hi_u32 s3, s4, s3
	s_add_i32 s4, s4, s3
	s_mul_hi_u32 s3, s4, 0x330
	s_mul_i32 s3, s3, s0
	s_sub_i32 s3, 0x330, s3
	s_sub_i32 s4, s3, s0
	s_cmp_ge_u32 s3, s0
	s_cselect_b32 s3, s4, s3
	s_sub_i32 s4, s3, s0
	s_cmp_ge_u32 s3, s0
	s_cselect_b32 s0, s4, s3
	s_cmp_eq_u32 s0, 0
	s_cselect_b64 s[4:5], -1, 0
	s_cmp_lt_i32 s2, s0
	s_cselect_b64 s[6:7], -1, 0
	s_or_b64 s[4:5], s[4:5], s[6:7]
	s_and_b64 vcc, exec, s[4:5]
	s_cbranch_vccnz .LBB0_1861
	v_and_b32_e32 v2, 0x7c, v218
	v_lshlrev_b32_e32 v3, 5, v0
	s_movk_i32 s0, 0x400
	v_and_or_b32 v12, v3, s0, v2
	v_bfe_u32 v2, v0, 3, 3
	v_lshl_or_b32 v4, v1, 5, v2
	v_lshlrev_b32_e32 v2, 3, v0
	v_lshl_add_u32 v11, v182, 4, 0
	v_and_b32_e32 v2, 56, v2
	v_mul_u32_u24_e32 v16, 0x2020, v1
	v_mov_b32_e32 v3, 0
	s_waitcnt vmcnt(0)
	v_lshl_add_u32 v27, v4, 2, 0
	v_mul_u32_u24_e32 v28, 0x404, v2
	v_lshlrev_b32_e32 v10, 6, v4
	s_add_i32 s10, 0, 0x22c38
	v_add_u32_e32 v16, v11, v16
	v_and_b32_e32 v13, 0xfc, v218
	v_and_b32_e32 v14, 56, v179
	s_mov_b32 s3, 11
	s_mov_b32 s91, 0
	v_or_b32_e32 v4, 0x200, v10
	v_mov_b32_e32 v5, v3
	v_or_b32_e32 v6, 0x400, v10
	v_mov_b32_e32 v7, v3
	v_or_b32_e32 v8, 0x600, v10
	v_mov_b32_e32 v9, v3
	v_mov_b32_e32 v15, s10
	s_movk_i32 s11, 0x1517
	s_movk_i32 s12, 0x800
	s_mov_b32 s13, 0x1104e000
	s_movk_i32 s14, -1304
	v_add_u32_e32 v17, 0x404, v16
	v_add_u32_e32 v18, 0x40c, v16
	v_add_u32_e32 v19, 0x808, v16
	v_add_u32_e32 v20, 0xc0c, v16
	v_add_u32_e32 v21, 0xc14, v16
	v_add_u32_e32 v22, 0x1414, v16
	v_add_u32_e32 v23, 0x141c, v16
	v_add_u32_e32 v24, 0x1818, v16
	v_add_u32_e32 v25, 0x1c1c, v16
	v_add_u32_e32 v26, 0x1c24, v16
	v_lshlrev_b32_e32 v2, 1, v2
	v_add_u32_e32 v27, v27, v28
	v_lshlrev_b32_e32 v10, 1, v10
	s_branch .LBB0_1854

; __device__ __forceinline__ unsigned g8_cvt_pk(float lo, float hi) { unsigned r; asm volatile("v_cvt_pk_bf16_f32 %0, %1, %2" : "=v"(r) : "v"(lo), "v"(hi)); return r; }
; __device__ __forceinline__ void convert_deferred(const Ptrs& P, unsigned char* lds, int quota) {
;     ...
;         const int t = *slot;
;         if (t >= DEF_GU + DEF_DN) break;
;         const bool gu = t < DEF_GU;
;         const float* src = gu ? P.in[34] : P.in[36]; bf16* dst = (bf16*)(P.ws + (gu ? WS_WGU : WS_WDN));
;         const int N = gu ? 2048 : 1024, ntn = N / 256, it = gu ? 2 * NE * 16 * 8 - DEF_GU + t : 2 * NE * 16 * 4 - DEF_DN + (t - DEF_GU);
;         f32x4 cur[8];
;         bt_load(src, N, gu ? 1 : 0, it, ntn, cur);
; #pragma unroll
;         for (int i = 0; i < 8; ++i) { float* tp = tile + (wid * 8 + i) * 257 + lane * 4; tp[0] = cur[i][0]; tp[1] = cur[i][1]; tp[2] = cur[i][2]; tp[3] = cur[i][3]; }
;         __syncthreads();
;         const int per = 16 * ntn, z = it / per, r = it % per, kt = r / ntn, nt = r % ntn;
;         bf16* d = dst + (size_t)z * N * 1024 + (((size_t)nt * 16 + kt) << 14);
;         const int kc = lane & 7;
; #pragma unroll
;         for (int pss = 0; pss < 4; ++pss) {
;             const int nn = wid * 32 + pss * 8 + (lane >> 3); float f[8];
; #pragma unroll
;             for (int j = 0; j < 8; ++j) f[j] = tile[(kc * 8 + j) * 257 + nn];
;             u32x4 w; w.x = g8_cvt_pk(f[0], f[1]); w.y = g8_cvt_pk(f[2], f[3]); w.z = g8_cvt_pk(f[4], f[5]); w.w = g8_cvt_pk(f[6], f[7]);
;             *(u32x4*)(d + nn * 64 + kc * 8) = w;
;         }
.LBB0_1858:
	s_or_b64 exec, exec, s[4:5]
	s_waitcnt lgkmcnt(0)
	s_barrier
	ds_read_b32 v11, v15
	s_mov_b64 s[4:5], -1
	s_waitcnt lgkmcnt(0)
	v_cmp_lt_i32_e32 vcc, s11, v11
	v_readfirstlane_b32 s0, v11
	s_cbranch_vccnz .LBB0_1853
	s_cmpk_gt_i32 s0, 0xe0f
	s_cselect_b64 vcc, -1, 0
	s_and_b64 s[4:5], vcc, exec
	s_cselect_b32 s4, s13, 0x104e000
	s_cselect_b32 s9, 0x400, s12
	s_cselect_b32 s15, s73, s69
	s_cselect_b32 s20, s72, s68
	s_cselect_b32 s5, s14, 0x11f0
	s_cselect_b32 s16, 20, 21
	s_cselect_b32 s21, 10, 11
	s_add_u32 s22, s78, s4
	s_addc_u32 s23, s79, 0
	s_lshr_b32 s6, s9, 4
	s_abs_i32 s4, s6
	v_cvt_f32_u32_e32 v11, s4
	s_sub_i32 s17, 0, s4
	s_add_i32 s5, s5, s0
	s_abs_i32 s7, s5
	v_rcp_iflag_f32_e32 v11, v11
	s_xor_b32 s0, s5, s6
	s_lshr_b32 s8, s9, 8
	s_ashr_i32 s0, s0, 31
	v_mul_f32_e32 v11, 0x4f7ffffe, v11
	v_cvt_u32_f32_e32 v11, v11
	s_nop 0
	v_readfirstlane_b32 s24, v11
	s_mul_i32 s17, s17, s24
	s_mul_hi_u32 s17, s24, s17
	s_add_i32 s24, s24, s17
	s_mul_hi_u32 s17, s7, s24
	s_mul_i32 s24, s17, s4
	s_sub_i32 s7, s7, s24
	s_add_i32 s24, s17, 1
	s_sub_i32 s25, s7, s4
	s_cmp_ge_u32 s7, s4
	s_cselect_b32 s17, s24, s17
	s_cselect_b32 s7, s25, s7
	s_add_i32 s24, s17, 1
	s_cmp_ge_u32 s7, s4
	s_cselect_b32 s4, s24, s17
	s_xor_b32 s4, s4, s0
	s_sub_i32 s4, s4, s0
	s_sext_i32_i8 s0, s8
	v_cvt_f32_i32_e32 v11, s0
	s_mul_i32 s6, s4, s6
	s_sub_i32 s5, s5, s6
	v_cvt_f32_i32_e32 v28, s5
	v_rcp_iflag_f32_e32 v29, v11
	s_xor_b32 s0, s5, s0
	s_ashr_i32 s0, s0, 30
	s_or_b32 s0, s0, 1
	v_mul_f32_e32 v29, v28, v29
	v_trunc_f32_e32 v29, v29
	v_fma_f32 v28, -v29, v11, v28
	v_cvt_i32_f32_e32 v29, v29
	v_cmp_ge_f32_e64 s[6:7], |v28|, |v11|
	s_and_b64 s[6:7], s[6:7], exec
	s_cselect_b32 s0, s0, 0
	v_readfirstlane_b32 s6, v29
	s_add_i32 s6, s6, s0
	s_mul_i32 s7, s6, s8
	s_sub_i32 s8, s5, s7
	s_sext_i32_i8 s5, s8
	v_lshl_add_u32 v11, s5, 7, v12
	v_lshl_or_b32 v28, s5, 8, v13
	s_ashr_i32 s5, s4, 31
	s_sext_i32_i8 s0, s6
	s_lshl_b64 s[16:17], s[4:5], s16
	v_lshl_or_b32 v30, s0, 6, v14
	s_lshl_b64 s[16:17], s[16:17], 2
	v_ashrrev_i32_e32 v31, 31, v30
	s_add_u32 s16, s20, s16
	v_cndmask_b32_e32 v28, v11, v28, vcc
	s_addc_u32 s17, s15, s17
	v_lshlrev_b64 v[30:31], s21, v[30:31]
	v_lshl_add_u64 v[30:31], v[30:31], 2, s[16:17]
	v_ashrrev_i32_e32 v29, 31, v28
	v_lshl_add_u64 v[52:53], v[28:29], 2, v[30:31]
	s_lshl_b64 s[16:17], 12, s21
	s_lshl_b32 s0, s9, 2
	v_lshl_add_u64 v[40:41], v[52:53], 0, s[16:17]
	s_lshl_b64 s[16:17], 24, s21
	v_lshl_add_u64 v[36:37], v[52:53], 0, s[0:1]
	v_lshl_add_u64 v[44:45], v[52:53], 0, s[16:17]
	s_lshl_b64 s[16:17], 28, s21
	v_lshl_add_u64 v[54:55], v[36:37], 0, s[0:1]
	v_lshl_add_u64 v[48:49], v[52:53], 0, s[16:17]
	s_lshl_b32 s0, s9, 3
	s_lshl_b64 s[16:17], 20, s21
	global_load_dwordx4 v[28:31], v[52:53], off nt
	global_load_dwordx4 v[32:35], v[36:37], off nt
	s_nop 0
	global_load_dwordx4 v[36:39], v[54:55], off nt
	s_nop 0
	global_load_dwordx4 v[40:43], v[40:41], off nt
	v_lshl_add_u64 v[54:55], v[54:55], 0, s[0:1]
	v_lshl_add_u64 v[56:57], v[52:53], 0, s[16:17]
	global_load_dwordx4 v[44:47], v[44:45], off nt
	s_nop 0
	global_load_dwordx4 v[48:51], v[48:49], off nt
	s_nop 0
	global_load_dwordx4 v[52:55], v[54:55], off nt
	s_nop 0
	global_load_dwordx4 v[56:59], v[56:57], off nt
	s_lshl_b64 s[4:5], s[4:5], s21
	s_lshl_b64 s[4:5], s[4:5], 11
	s_add_u32 s0, s22, s4
	s_addc_u32 s9, s23, s5
	s_bfe_i64 s[4:5], s[8:9], 0x80000
	s_bfe_i64 s[6:7], s[6:7], 0x80000
	s_lshl_b64 s[4:5], s[4:5], 19
	s_add_u32 s0, s0, s4
	s_addc_u32 s8, s9, s5
	s_lshl_b64 s[4:5], s[6:7], 15
	s_add_u32 s4, s0, s4
	s_addc_u32 s5, s8, s5
	v_mov_b32_e32 v11, v3
	s_add_i32 s3, s3, -1
	s_cmp_eq_u32 s3, 0
	s_waitcnt vmcnt(7)
	ds_write_b128 v16, v[28:31]
	s_waitcnt vmcnt(6)
	ds_write2_b32 v17, v32, v33 offset1:1
	ds_write2_b32 v18, v34, v35 offset1:1
	s_waitcnt vmcnt(3)
	ds_write2_b64 v24, v[44:45], v[46:47] offset1:1
	s_waitcnt vmcnt(2)
	ds_write2_b32 v25, v48, v49 offset1:1
	ds_write2_b32 v26, v50, v51 offset1:1
	ds_write2_b64 v19, v[36:37], v[38:39] offset1:1
	ds_write2_b32 v20, v40, v41 offset1:1
	ds_write2_b32 v21, v42, v43 offset1:1
	s_waitcnt vmcnt(1)
	ds_write_b128 v16, v[52:55] offset:4112
	s_waitcnt vmcnt(0)
	ds_write2_b32 v22, v56, v57 offset1:1
	ds_write2_b32 v23, v58, v59 offset1:1
	s_waitcnt lgkmcnt(0)
	s_barrier
	ds_read_b32 v28, v27 offset:1028
	ds_read_b32 v29, v27 offset:3084
	ds_read_b32 v30, v27 offset:5140
	ds_read_b32 v31, v27 offset:7196
	ds_read_b32 v32, v27 offset:6168
	ds_read_b32 v33, v27 offset:4112
	ds_read_b32 v34, v27 offset:2056
	ds_read_b32 v35, v27
	s_waitcnt lgkmcnt(0)
	v_cvt_pk_bf16_f32 v28, v35, v28
	v_cvt_pk_bf16_f32 v29, v34, v29
	v_cvt_pk_bf16_f32 v30, v33, v30
	v_cvt_pk_bf16_f32 v31, v32, v31
	ds_read_b32 v36, v27 offset:1060
	ds_read_b32 v37, v27 offset:3116
	ds_read_b32 v38, v27 offset:5172
	ds_read_b32 v39, v27 offset:7228
	ds_read_b32 v40, v27 offset:6200
	ds_read_b32 v41, v27 offset:4144
	ds_read_b32 v42, v27 offset:2088
	ds_read_b32 v43, v27 offset:32
	v_lshl_add_u64 v[32:33], s[4:5], 0, v[2:3]
	v_lshl_add_u64 v[34:35], v[32:33], 0, v[10:11]
	global_store_dwordx4 v[34:35], v[28:31], off
	v_lshl_add_u64 v[34:35], v[4:5], 1, v[32:33]
	s_cselect_b64 s[4:5], -1, 0
	s_waitcnt lgkmcnt(0)
	v_cvt_pk_bf16_f32 v28, v43, v36
	v_cvt_pk_bf16_f32 v29, v42, v37
	v_cvt_pk_bf16_f32 v30, v41, v38
	v_cvt_pk_bf16_f32 v31, v40, v39
	ds_read_b32 v11, v27 offset:1092
	ds_read_b32 v36, v27 offset:3148
	ds_read_b32 v37, v27 offset:6232
	ds_read_b32 v38, v27 offset:4176
	ds_read_b32 v39, v27 offset:2120
	ds_read_b32 v40, v27 offset:64
	ds_read_b32 v41, v27 offset:5204
	ds_read_b32 v42, v27 offset:7260
	global_store_dwordx4 v[34:35], v[28:31], off
	v_lshl_add_u64 v[34:35], v[6:7], 1, v[32:33]
	v_lshl_add_u64 v[32:33], v[8:9], 1, v[32:33]
	s_waitcnt lgkmcnt(2)
	v_cvt_pk_bf16_f32 v28, v40, v11
	v_cvt_pk_bf16_f32 v29, v39, v36
	s_waitcnt lgkmcnt(1)
	v_cvt_pk_bf16_f32 v30, v38, v41
	s_waitcnt lgkmcnt(0)
	v_cvt_pk_bf16_f32 v31, v37, v42
	ds_read_b32 v11, v27 offset:1124
	ds_read_b32 v36, v27 offset:3180
	ds_read_b32 v37, v27 offset:6264
	ds_read_b32 v38, v27 offset:4208
	ds_read_b32 v39, v27 offset:2152
	ds_read_b32 v40, v27 offset:96
	ds_read_b32 v41, v27 offset:5236
	ds_read_b32 v42, v27 offset:7292
	global_store_dwordx4 v[34:35], v[28:31], off
	s_waitcnt lgkmcnt(2)
	s_nop 0
	v_cvt_pk_bf16_f32 v28, v40, v11
	v_cvt_pk_bf16_f32 v29, v39, v36
	s_waitcnt lgkmcnt(1)
	v_cvt_pk_bf16_f32 v30, v38, v41
	s_waitcnt lgkmcnt(0)
	v_cvt_pk_bf16_f32 v31, v37, v42
	global_store_dwordx4 v[32:33], v[28:31], off
	s_branch .LBB0_1853

; #define SEAM(k) do { if (IN(k) && IN((k) + 1)) xcd_barrier(bar); \
;         if (PROBE_MASK) { const unsigned long long t_ = __builtin_amdgcn_s_memrealtime(); if ((PROBE_MASK >> (k)) & 1u) pr_acc += t_ - pr_t0; pr_t0 = t_; } } while (0)
; __device__ __forceinline__ void convert_deferred(const Ptrs& P, unsigned char* lds, int quota) {
;     const int tid = threadIdx.x, wid = tid >> 6, lane = tid & 63;
;     float* tile = (float*)lds;
;     volatile __attribute__((address_space(3))) int* slot = (volatile __attribute__((address_space(3))) int*)((__attribute__((address_space(3))) unsigned char*)lds + 131072 + 320 + 11000);
;     unsigned* q = (unsigned*)(P.ws + WS_CTL) + CW_DEFQ;
;     for (int n = 0; n < quota; ++n) {
;         __syncthreads();
;         if (tid == 0) *slot = (int)atomicAdd(q, 1u);
;         __syncthreads();
;         const int t = *slot;
;         if (t >= DEF_GU + DEF_DN) break;
;         const bool gu = t < DEF_GU;
;         const float* src = gu ? P.in[34] : P.in[36]; bf16* dst = (bf16*)(P.ws + (gu ? WS_WGU : WS_WDN));
;         const int N = gu ? 2048 : 1024, ntn = N / 256, it = gu ? 2 * NE * 16 * 8 - DEF_GU + t : 2 * NE * 16 * 4 - DEF_DN + (t - DEF_GU);
; __global__ void __launch_bounds__(NT, 2) mega(Args args) {
;     ...
;     if (IN(15)) { ph_norm2_router(P, lds, 1, 1); convert_deferred(P, lds, 1 << 20); } SEAM(15);
.LBB0_2278:
	v_and_b32_e32 v2, 0x7c, v179
	v_lshlrev_b32_e32 v3, 5, v0
	s_movk_i32 s0, 0x400
	v_and_or_b32 v12, v3, s0, v2
	v_lshrrev_b32_e32 v2, 3, v0
	v_and_b32_e32 v14, 56, v2
	v_lshrrev_b32_e32 v2, 3, v182
	v_lshl_or_b32 v4, v1, 5, v2
	v_lshl_add_u32 v5, v182, 4, 0
	v_and_b32_e32 v2, 56, v188
	v_lshl_add_u32 v7, v4, 2, 0
	v_mul_u32_u24_e32 v11, 0x2020, v1
	v_lshlrev_b32_e32 v4, 6, v4
	v_mul_u32_u24_e32 v9, 0x404, v2
	v_or_b32_e32 v6, 0x200, v4
	v_or_b32_e32 v8, 0x400, v4
	v_or_b32_e32 v10, 0x600, v4
	s_add_i32 s10, 0, 0x22c38
	v_add_u32_e32 v16, v5, v11
	v_and_b32_e32 v13, 0xfc, v179
	s_mov_b32 s1, 0
	v_mov_b32_e32 v3, 0
	s_mov_b32 s3, 0x100000
	v_mov_b32_e32 v15, s10
	s_movk_i32 s11, 0x1517
	s_movk_i32 s12, 0x800
	s_mov_b32 s13, 0x1104e000
	s_movk_i32 s14, -1304
	v_add_u32_e32 v17, 0x404, v16
	v_add_u32_e32 v18, 0x40c, v16
	v_add_u32_e32 v19, 0x808, v16
	v_add_u32_e32 v20, 0xc0c, v16
	v_add_u32_e32 v21, 0xc14, v16
	v_add_u32_e32 v22, 0x1414, v16
	v_add_u32_e32 v23, 0x141c, v16
	v_add_u32_e32 v24, 0x1818, v16
	v_add_u32_e32 v25, 0x1c1c, v16
	v_add_u32_e32 v26, 0x1c24, v16
	v_lshlrev_b32_e32 v2, 1, v2
	v_add_u32_e32 v27, v7, v9
	v_lshlrev_b32_e32 v4, 1, v4
	v_lshlrev_b32_e32 v6, 1, v6
	v_lshlrev_b32_e32 v8, 1, v8
	v_lshlrev_b32_e32 v10, 1, v10
	s_branch .LBB0_2280

; __device__ __forceinline__ unsigned g8_cvt_pk(float lo, float hi) { unsigned r; asm volatile("v_cvt_pk_bf16_f32 %0, %1, %2" : "=v"(r) : "v"(lo), "v"(hi)); return r; }
; __device__ __forceinline__ void convert_deferred(const Ptrs& P, unsigned char* lds, int quota) {
;     ...
;         const int t = *slot;
;         if (t >= DEF_GU + DEF_DN) break;
;         const bool gu = t < DEF_GU;
;         const float* src = gu ? P.in[34] : P.in[36]; bf16* dst = (bf16*)(P.ws + (gu ? WS_WGU : WS_WDN));
;         const int N = gu ? 2048 : 1024, ntn = N / 256, it = gu ? 2 * NE * 16 * 8 - DEF_GU + t : 2 * NE * 16 * 4 - DEF_DN + (t - DEF_GU);
;         f32x4 cur[8];
;         bt_load(src, N, gu ? 1 : 0, it, ntn, cur);
; #pragma unroll
;         for (int i = 0; i < 8; ++i) { float* tp = tile + (wid * 8 + i) * 257 + lane * 4; tp[0] = cur[i][0]; tp[1] = cur[i][1]; tp[2] = cur[i][2]; tp[3] = cur[i][3]; }
;         __syncthreads();
;         const int per = 16 * ntn, z = it / per, r = it % per, kt = r / ntn, nt = r % ntn;
;         bf16* d = dst + (size_t)z * N * 1024 + (((size_t)nt * 16 + kt) << 14);
;         const int kc = lane & 7;
; #pragma unroll
;         for (int pss = 0; pss < 4; ++pss) {
;             const int nn = wid * 32 + pss * 8 + (lane >> 3); float f[8];
; #pragma unroll
;             for (int j = 0; j < 8; ++j) f[j] = tile[(kc * 8 + j) * 257 + nn];
;             u32x4 w; w.x = g8_cvt_pk(f[0], f[1]); w.y = g8_cvt_pk(f[2], f[3]); w.z = g8_cvt_pk(f[4], f[5]); w.w = g8_cvt_pk(f[6], f[7]);
;             *(u32x4*)(d + nn * 64 + kc * 8) = w;
;         }
.LBB0_2284:
	s_or_b64 exec, exec, s[4:5]
	s_waitcnt lgkmcnt(0)
	s_barrier
	ds_read_b32 v5, v15
	s_mov_b64 s[4:5], -1
	s_waitcnt lgkmcnt(0)
	v_cmp_lt_i32_e32 vcc, s11, v5
	v_readfirstlane_b32 s0, v5
	s_cbranch_vccnz .LBB0_2279
	s_cmpk_gt_i32 s0, 0xe0f
	s_cselect_b64 vcc, -1, 0
	s_and_b64 s[4:5], vcc, exec
	s_cselect_b32 s4, s13, 0x104e000
	s_cselect_b32 s9, 0x400, s12
	s_cselect_b32 s15, s73, s69
	s_cselect_b32 s18, s72, s68
	s_cselect_b32 s5, s14, 0x11f0
	s_cselect_b32 s16, 20, 21
	s_cselect_b32 s19, 10, 11
	s_add_u32 s22, s78, s4
	s_addc_u32 s23, s79, 0
	s_lshr_b32 s6, s9, 4
	s_abs_i32 s4, s6
	v_cvt_f32_u32_e32 v5, s4
	s_sub_i32 s17, 0, s4
	s_add_i32 s5, s5, s0
	s_abs_i32 s7, s5
	v_rcp_iflag_f32_e32 v5, v5
	s_xor_b32 s0, s5, s6
	s_lshr_b32 s8, s9, 8
	s_ashr_i32 s0, s0, 31
	v_mul_f32_e32 v5, 0x4f7ffffe, v5
	v_cvt_u32_f32_e32 v5, v5
	s_nop 0
	v_readfirstlane_b32 s24, v5
	s_mul_i32 s17, s17, s24
	s_mul_hi_u32 s17, s24, s17
	s_add_i32 s24, s24, s17
	s_mul_hi_u32 s17, s7, s24
	s_mul_i32 s24, s17, s4
	s_sub_i32 s7, s7, s24
	s_add_i32 s24, s17, 1
	s_sub_i32 s25, s7, s4
	s_cmp_ge_u32 s7, s4
	s_cselect_b32 s17, s24, s17
	s_cselect_b32 s7, s25, s7
	s_add_i32 s24, s17, 1
	s_cmp_ge_u32 s7, s4
	s_cselect_b32 s4, s24, s17
	s_xor_b32 s4, s4, s0
	s_sub_i32 s4, s4, s0
	s_sext_i32_i8 s0, s8
	v_cvt_f32_i32_e32 v5, s0
	s_mul_i32 s6, s4, s6
	s_sub_i32 s5, s5, s6
	v_cvt_f32_i32_e32 v7, s5
	v_rcp_iflag_f32_e32 v9, v5
	s_xor_b32 s0, s5, s0
	s_ashr_i32 s0, s0, 30
	s_or_b32 s0, s0, 1
	v_mul_f32_e32 v9, v7, v9
	v_trunc_f32_e32 v9, v9
	v_fma_f32 v7, -v9, v5, v7
	v_cvt_i32_f32_e32 v9, v9
	v_cmp_ge_f32_e64 s[6:7], |v7|, |v5|
	s_and_b64 s[6:7], s[6:7], exec
	s_cselect_b32 s0, s0, 0
	v_readfirstlane_b32 s6, v9
	s_add_i32 s6, s6, s0
	s_mul_i32 s7, s6, s8
	s_sub_i32 s8, s5, s7
	s_sext_i32_i8 s5, s8
	v_lshl_add_u32 v5, s5, 7, v12
	v_lshl_or_b32 v7, s5, 8, v13
	s_ashr_i32 s5, s4, 31
	s_sext_i32_i8 s0, s6
	s_lshl_b64 s[16:17], s[4:5], s16
	v_lshl_or_b32 v30, s0, 6, v14
	s_lshl_b64 s[16:17], s[16:17], 2
	v_ashrrev_i32_e32 v31, 31, v30
	s_add_u32 s16, s18, s16
	v_cndmask_b32_e32 v28, v5, v7, vcc
	s_addc_u32 s17, s15, s17
	v_lshlrev_b64 v[30:31], s19, v[30:31]
	v_lshl_add_u64 v[30:31], v[30:31], 2, s[16:17]
	v_ashrrev_i32_e32 v29, 31, v28
	v_lshl_add_u64 v[52:53], v[28:29], 2, v[30:31]
	s_lshl_b32 s0, s9, 2
	s_lshl_b64 s[16:17], 12, s19
	v_lshl_add_u64 v[36:37], v[52:53], 0, s[0:1]
	v_lshl_add_u64 v[44:45], v[52:53], 0, s[16:17]
	s_lshl_b64 s[16:17], 24, s19
	v_lshl_add_u64 v[54:55], v[36:37], 0, s[0:1]
	v_lshl_add_u64 v[56:57], v[52:53], 0, s[16:17]
	s_lshl_b64 s[16:17], 28, s19
	s_lshl_b32 s0, s9, 3
	v_lshl_add_u64 v[58:59], v[52:53], 0, s[16:17]
	v_lshl_add_u64 v[60:61], v[54:55], 0, s[0:1]
	s_lshl_b64 s[16:17], 20, s19
	global_load_dwordx4 v[28:31], v[52:53], off nt
	global_load_dwordx4 v[32:35], v[36:37], off nt
	s_nop 0
	global_load_dwordx4 v[36:39], v[54:55], off nt
	global_load_dwordx4 v[40:43], v[44:45], off nt
	s_nop 0
	global_load_dwordx4 v[44:47], v[56:57], off nt
	global_load_dwordx4 v[48:51], v[58:59], off nt
	v_lshl_add_u64 v[62:63], v[52:53], 0, s[16:17]
	global_load_dwordx4 v[52:55], v[60:61], off nt
	global_load_dwordx4 v[56:59], v[62:63], off nt
	s_lshl_b64 s[4:5], s[4:5], s19
	s_lshl_b64 s[4:5], s[4:5], 11
	s_add_u32 s0, s22, s4
	s_addc_u32 s9, s23, s5
	s_bfe_i64 s[4:5], s[8:9], 0x80000
	s_bfe_i64 s[6:7], s[6:7], 0x80000
	s_lshl_b64 s[4:5], s[4:5], 19
	s_add_u32 s0, s0, s4
	s_addc_u32 s8, s9, s5
	s_lshl_b64 s[4:5], s[6:7], 15
	s_add_u32 s4, s0, s4
	s_addc_u32 s5, s8, s5
	v_mov_b32_e32 v5, v3
	s_add_i32 s3, s3, -1
	s_cmp_eq_u32 s3, 0
	s_waitcnt vmcnt(7)
	ds_write_b128 v16, v[28:31]
	s_waitcnt vmcnt(6)
	ds_write2_b32 v17, v32, v33 offset1:1
	ds_write2_b32 v18, v34, v35 offset1:1
	s_waitcnt vmcnt(3)
	ds_write2_b64 v24, v[44:45], v[46:47] offset1:1
	s_waitcnt vmcnt(2)
	ds_write2_b32 v25, v48, v49 offset1:1
	ds_write2_b32 v26, v50, v51 offset1:1
	ds_write2_b64 v19, v[36:37], v[38:39] offset1:1
	ds_write2_b32 v20, v40, v41 offset1:1
	ds_write2_b32 v21, v42, v43 offset1:1
	s_waitcnt vmcnt(1)
	ds_write_b128 v16, v[52:55] offset:4112
	s_waitcnt vmcnt(0)
	ds_write2_b32 v22, v56, v57 offset1:1
	ds_write2_b32 v23, v58, v59 offset1:1
	s_waitcnt lgkmcnt(0)
	s_barrier
	ds_read_b32 v7, v27 offset:1028
	ds_read_b32 v9, v27 offset:3084
	ds_read_b32 v11, v27 offset:5140
	ds_read_b32 v31, v27 offset:7196
	ds_read_b32 v32, v27 offset:6168
	ds_read_b32 v30, v27 offset:4112
	ds_read_b32 v29, v27 offset:2056
	ds_read_b32 v28, v27
	s_waitcnt lgkmcnt(0)
	v_cvt_pk_bf16_f32 v28, v28, v7
	v_cvt_pk_bf16_f32 v29, v29, v9
	v_cvt_pk_bf16_f32 v30, v30, v11
	v_cvt_pk_bf16_f32 v31, v32, v31
	ds_read_b32 v7, v27 offset:1060
	ds_read_b32 v9, v27 offset:3116
	ds_read_b32 v11, v27 offset:5172
	ds_read_b32 v36, v27 offset:7228
	ds_read_b32 v37, v27 offset:6200
	ds_read_b32 v38, v27 offset:4144
	ds_read_b32 v39, v27 offset:2088
	ds_read_b32 v40, v27 offset:32
	v_lshl_add_u64 v[32:33], s[4:5], 0, v[2:3]
	v_lshl_add_u64 v[34:35], v[32:33], 0, v[4:5]
	global_store_dwordx4 v[34:35], v[28:31], off
	s_cselect_b64 s[4:5], -1, 0
	s_waitcnt lgkmcnt(0)
	v_cvt_pk_bf16_f32 v28, v40, v7
	v_cvt_pk_bf16_f32 v29, v39, v9
	v_cvt_pk_bf16_f32 v30, v38, v11
	v_cvt_pk_bf16_f32 v31, v37, v36
	ds_read_b32 v5, v27 offset:1092
	ds_read_b32 v9, v27 offset:3148
	ds_read_b32 v11, v27 offset:5204
	ds_read_b32 v36, v27 offset:6232
	ds_read_b32 v37, v27 offset:4176
	ds_read_b32 v38, v27 offset:2120
	ds_read_b32 v39, v27 offset:64
	ds_read_b32 v40, v27 offset:7260
	v_mov_b32_e32 v7, v3
	v_lshl_add_u64 v[34:35], v[32:33], 0, v[6:7]
	global_store_dwordx4 v[34:35], v[28:31], off
	s_waitcnt lgkmcnt(1)
	s_nop 0
	v_cvt_pk_bf16_f32 v28, v39, v5
	v_cvt_pk_bf16_f32 v29, v38, v9
	v_cvt_pk_bf16_f32 v30, v37, v11
	s_waitcnt lgkmcnt(0)
	v_cvt_pk_bf16_f32 v31, v36, v40
	ds_read_b32 v5, v27 offset:1124
	ds_read_b32 v7, v27 offset:3180
	ds_read_b32 v11, v27 offset:5236
	ds_read_b32 v36, v27 offset:6264
	ds_read_b32 v37, v27 offset:4208
	ds_read_b32 v38, v27 offset:2152
	ds_read_b32 v39, v27 offset:96
	ds_read_b32 v40, v27 offset:7292
	v_mov_b32_e32 v9, v3
	v_lshl_add_u64 v[34:35], v[32:33], 0, v[8:9]
	global_store_dwordx4 v[34:35], v[28:31], off
	s_waitcnt lgkmcnt(1)
	s_nop 0
	v_cvt_pk_bf16_f32 v28, v39, v5
	v_cvt_pk_bf16_f32 v29, v38, v7
	v_cvt_pk_bf16_f32 v30, v37, v11
	v_mov_b32_e32 v11, v3
	v_lshl_add_u64 v[32:33], v[32:33], 0, v[10:11]
	s_waitcnt lgkmcnt(0)
	v_cvt_pk_bf16_f32 v31, v36, v40
	global_store_dwordx4 v[32:33], v[28:31], off
	s_branch .LBB0_2279
